# speedup vs baseline: 1.0343x; 1.0343x over previous
_Z4k_lnPKfS0_S0_PDF16_PfS2_7CvtArgs:
	s_cmpk_lt_u32 s2, 0x100
	s_mov_b64 s[4:5], -1
	s_cbranch_scc0 .LBB0_8
	s_load_dwordx8 s[4:11], s[0:1], 0x0
	s_load_dwordx4 s[12:15], s[0:1], 0x20
	s_lshr_b32 s16, s2, 7
	s_lshl_b32 s3, s2, 5
	s_mov_b32 s17, 0
	s_and_b32 s3, s3, 0xfe0
	s_lshl_b64 s[18:19], s[16:17], 23
	v_and_b32_e32 v8, 0x1e0, v0
	v_and_b32_e32 v1, 31, v0
	v_lshlrev_b32_e32 v4, 2, v1
	v_mov_b32_e32 v5, 0
	v_lshl_add_u32 v9, v8, 14, v4
	v_lshlrev_b32_e32 v3, 2, v8
	v_mov_b32_e32 v6, 0
	v_mov_b32_e32 v7, 0
	s_waitcnt lgkmcnt(0)
	s_add_u32 s18, s4, s18
	s_addc_u32 s19, s5, s19
	s_lshl_b32 s4, s3, 2
	s_add_u32 s18, s18, s4
	s_addc_u32 s19, s19, 0
	global_load_dwordx4 v[66:69], v3, s[6:7]
	global_load_dwordx4 v[82:85], v3, s[8:9]
	global_load_dwordx4 v[70:73], v3, s[6:7] offset:16
	global_load_dwordx4 v[86:89], v3, s[8:9] offset:16
	global_load_dwordx4 v[74:77], v3, s[6:7] offset:32
	global_load_dwordx4 v[90:93], v3, s[8:9] offset:32
	global_load_dwordx4 v[78:81], v3, s[6:7] offset:48
	global_load_dwordx4 v[94:97], v3, s[8:9] offset:48
	global_load_dword v34, v9, s[18:19] nt
	s_add_u32 s18, s18, 0x4000
	s_addc_u32 s19, s19, 0
	global_load_dword v35, v9, s[18:19] nt
	s_add_u32 s18, s18, 0x4000
	s_addc_u32 s19, s19, 0
	global_load_dword v36, v9, s[18:19] nt
	s_add_u32 s18, s18, 0x4000
	s_addc_u32 s19, s19, 0
	global_load_dword v37, v9, s[18:19] nt
	s_add_u32 s18, s18, 0x4000
	s_addc_u32 s19, s19, 0
	global_load_dword v38, v9, s[18:19] nt
	s_add_u32 s18, s18, 0x4000
	s_addc_u32 s19, s19, 0
	global_load_dword v39, v9, s[18:19] nt
	s_add_u32 s18, s18, 0x4000
	s_addc_u32 s19, s19, 0
	global_load_dword v40, v9, s[18:19] nt
	s_add_u32 s18, s18, 0x4000
	s_addc_u32 s19, s19, 0
	global_load_dword v41, v9, s[18:19] nt
	s_add_u32 s18, s18, 0x4000
	s_addc_u32 s19, s19, 0
	global_load_dword v42, v9, s[18:19] nt
	s_add_u32 s18, s18, 0x4000
	s_addc_u32 s19, s19, 0
	global_load_dword v43, v9, s[18:19] nt
	s_add_u32 s18, s18, 0x4000
	s_addc_u32 s19, s19, 0
	global_load_dword v44, v9, s[18:19] nt
	s_add_u32 s18, s18, 0x4000
	s_addc_u32 s19, s19, 0
	global_load_dword v45, v9, s[18:19] nt
	s_add_u32 s18, s18, 0x4000
	s_addc_u32 s19, s19, 0
	global_load_dword v46, v9, s[18:19] nt
	s_add_u32 s18, s18, 0x4000
	s_addc_u32 s19, s19, 0
	global_load_dword v47, v9, s[18:19] nt
	s_add_u32 s18, s18, 0x4000
	s_addc_u32 s19, s19, 0
	global_load_dword v48, v9, s[18:19] nt
	s_add_u32 s18, s18, 0x4000
	s_addc_u32 s19, s19, 0
	global_load_dword v49, v9, s[18:19] nt
	s_add_u32 s18, s18, 0x4000
	s_addc_u32 s19, s19, 0
	global_load_dword v50, v9, s[18:19] nt
	s_add_u32 s18, s18, 0x4000
	s_addc_u32 s19, s19, 0
	global_load_dword v51, v9, s[18:19] nt
	s_add_u32 s18, s18, 0x4000
	s_addc_u32 s19, s19, 0
	global_load_dword v52, v9, s[18:19] nt
	s_add_u32 s18, s18, 0x4000
	s_addc_u32 s19, s19, 0
	global_load_dword v53, v9, s[18:19] nt
	s_add_u32 s18, s18, 0x4000
	s_addc_u32 s19, s19, 0
	global_load_dword v54, v9, s[18:19] nt
	s_add_u32 s18, s18, 0x4000
	s_addc_u32 s19, s19, 0
	global_load_dword v55, v9, s[18:19] nt
	s_add_u32 s18, s18, 0x4000
	s_addc_u32 s19, s19, 0
	global_load_dword v56, v9, s[18:19] nt
	s_add_u32 s18, s18, 0x4000
	s_addc_u32 s19, s19, 0
	global_load_dword v57, v9, s[18:19] nt
	s_add_u32 s18, s18, 0x4000
	s_addc_u32 s19, s19, 0
	global_load_dword v58, v9, s[18:19] nt
	s_add_u32 s18, s18, 0x4000
	s_addc_u32 s19, s19, 0
	global_load_dword v59, v9, s[18:19] nt
	s_add_u32 s18, s18, 0x4000
	s_addc_u32 s19, s19, 0
	global_load_dword v60, v9, s[18:19] nt
	s_add_u32 s18, s18, 0x4000
	s_addc_u32 s19, s19, 0
	global_load_dword v61, v9, s[18:19] nt
	s_add_u32 s18, s18, 0x4000
	s_addc_u32 s19, s19, 0
	global_load_dword v62, v9, s[18:19] nt
	s_add_u32 s18, s18, 0x4000
	s_addc_u32 s19, s19, 0
	global_load_dword v63, v9, s[18:19] nt
	s_add_u32 s18, s18, 0x4000
	s_addc_u32 s19, s19, 0
	global_load_dword v64, v9, s[18:19] nt
	s_add_u32 s18, s18, 0x4000
	s_addc_u32 s19, s19, 0
	global_load_dword v65, v9, s[18:19] nt
	s_waitcnt vmcnt(31)
	v_add_f32_e32 v6, v6, v34
	v_fmac_f32_e32 v7, v34, v34
	s_waitcnt vmcnt(30)
	v_add_f32_e32 v6, v6, v35
	v_fmac_f32_e32 v7, v35, v35
	s_waitcnt vmcnt(29)
	v_add_f32_e32 v6, v6, v36
	v_fmac_f32_e32 v7, v36, v36
	s_waitcnt vmcnt(28)
	v_add_f32_e32 v6, v6, v37
	v_fmac_f32_e32 v7, v37, v37
	s_waitcnt vmcnt(27)
	v_add_f32_e32 v6, v6, v38
	v_fmac_f32_e32 v7, v38, v38
	s_waitcnt vmcnt(26)
	v_add_f32_e32 v6, v6, v39
	v_fmac_f32_e32 v7, v39, v39
	s_waitcnt vmcnt(25)
	v_add_f32_e32 v6, v6, v40
	v_fmac_f32_e32 v7, v40, v40
	s_waitcnt vmcnt(24)
	v_add_f32_e32 v6, v6, v41
	v_fmac_f32_e32 v7, v41, v41
	s_waitcnt vmcnt(23)
	v_add_f32_e32 v6, v6, v42
	v_fmac_f32_e32 v7, v42, v42
	s_waitcnt vmcnt(22)
	v_add_f32_e32 v6, v6, v43
	v_fmac_f32_e32 v7, v43, v43
	s_waitcnt vmcnt(21)
	v_add_f32_e32 v6, v6, v44
	v_fmac_f32_e32 v7, v44, v44
	s_waitcnt vmcnt(20)
	v_add_f32_e32 v6, v6, v45
	v_fmac_f32_e32 v7, v45, v45
	s_waitcnt vmcnt(19)
	v_add_f32_e32 v6, v6, v46
	v_fmac_f32_e32 v7, v46, v46
	s_waitcnt vmcnt(18)
	v_add_f32_e32 v6, v6, v47
	v_fmac_f32_e32 v7, v47, v47
	s_waitcnt vmcnt(17)
	v_add_f32_e32 v6, v6, v48
	v_fmac_f32_e32 v7, v48, v48
	s_waitcnt vmcnt(16)
	v_add_f32_e32 v6, v6, v49
	v_fmac_f32_e32 v7, v49, v49
	s_waitcnt vmcnt(15)
	v_add_f32_e32 v6, v6, v50
	v_fmac_f32_e32 v7, v50, v50
	s_waitcnt vmcnt(14)
	v_add_f32_e32 v6, v6, v51
	v_fmac_f32_e32 v7, v51, v51
	s_waitcnt vmcnt(13)
	v_add_f32_e32 v6, v6, v52
	v_fmac_f32_e32 v7, v52, v52
	s_waitcnt vmcnt(12)
	v_add_f32_e32 v6, v6, v53
	v_fmac_f32_e32 v7, v53, v53
	s_waitcnt vmcnt(11)
	v_add_f32_e32 v6, v6, v54
	v_fmac_f32_e32 v7, v54, v54
	s_waitcnt vmcnt(10)
	v_add_f32_e32 v6, v6, v55
	v_fmac_f32_e32 v7, v55, v55
	s_waitcnt vmcnt(9)
	v_add_f32_e32 v6, v6, v56
	v_fmac_f32_e32 v7, v56, v56
	s_waitcnt vmcnt(8)
	v_add_f32_e32 v6, v6, v57
	v_fmac_f32_e32 v7, v57, v57
	s_waitcnt vmcnt(7)
	v_add_f32_e32 v6, v6, v58
	v_fmac_f32_e32 v7, v58, v58
	s_waitcnt vmcnt(6)
	v_add_f32_e32 v6, v6, v59
	v_fmac_f32_e32 v7, v59, v59
	s_waitcnt vmcnt(5)
	v_add_f32_e32 v6, v6, v60
	v_fmac_f32_e32 v7, v60, v60
	s_waitcnt vmcnt(4)
	v_add_f32_e32 v6, v6, v61
	v_fmac_f32_e32 v7, v61, v61
	s_waitcnt vmcnt(3)
	v_add_f32_e32 v6, v6, v62
	v_fmac_f32_e32 v7, v62, v62
	s_waitcnt vmcnt(2)
	v_add_f32_e32 v6, v6, v63
	v_fmac_f32_e32 v7, v63, v63
	s_waitcnt vmcnt(1)
	v_add_f32_e32 v6, v6, v64
	v_fmac_f32_e32 v7, v64, v64
	s_waitcnt vmcnt(0)
	v_add_f32_e32 v6, v6, v65
	v_fmac_f32_e32 v7, v65, v65
	v_lshlrev_b32_e32 v5, 2, v0
	s_movk_i32 s4, 0x780
	v_and_or_b32 v9, v5, s4, v4
	v_add_u32_e32 v9, 0x80, v9
	v_cmp_gt_u32_e32 vcc, 32, v0
	ds_write2st64_b32 v9, v7, v6 offset0:128 offset1:136
	s_waitcnt lgkmcnt(0)
	s_barrier
	s_and_saveexec_b64 s[18:19], vcc
	s_cbranch_execz .LBB0_5
	v_add_u32_e32 v9, 0x8800, v5
	ds_read2_b32 v[6:7], v9 offset0:32 offset1:64
	v_add_u32_e32 v18, 0x8000, v5
	ds_read2_b32 v[10:11], v18 offset0:32 offset1:64
	ds_read2_b32 v[12:13], v9 offset0:96 offset1:128
	ds_read2_b32 v[14:15], v18 offset0:96 offset1:128
	ds_read2_b32 v[16:17], v9 offset0:160 offset1:192
	ds_read2_b32 v[18:19], v18 offset0:160 offset1:192
	s_waitcnt lgkmcnt(4)
	v_mov_b32_e32 v20, v10
	v_add_u32_e32 v9, 0x8a00, v5
	v_mov_b32_e32 v21, v6
	v_pk_add_f32 v[20:21], v[20:21], 0 op_sel_hi:[1,0]
	v_mov_b32_e32 v6, v11
	v_pk_add_f32 v[6:7], v[20:21], v[6:7]
	s_waitcnt lgkmcnt(2)
	v_mov_b32_e32 v10, v14
	v_mov_b32_e32 v11, v12
	v_pk_add_f32 v[6:7], v[6:7], v[10:11]
	v_mov_b32_e32 v12, v15
	v_pk_add_f32 v[6:7], v[6:7], v[12:13]
	s_waitcnt lgkmcnt(0)
	v_mov_b32_e32 v10, v18
	v_mov_b32_e32 v11, v16
	v_pk_add_f32 v[6:7], v[6:7], v[10:11]
	ds_read2_b32 v[10:11], v9 offset0:96 offset1:128
	v_add_u32_e32 v9, 0x8200, v5
	ds_read2_b32 v[12:13], v9 offset0:96 offset1:128
	v_add_u32_e32 v9, 0x8c00, v5
	ds_read2_b32 v[14:15], v9 offset0:32 offset1:64
	v_add_u32_e32 v16, 0x8400, v5
	ds_read2_b32 v[20:21], v16 offset0:32 offset1:64
	ds_read2_b32 v[22:23], v9 offset0:96 offset1:128
	ds_read2_b32 v[24:25], v16 offset0:96 offset1:128
	ds_read2_b32 v[26:27], v9 offset0:160 offset1:192
	ds_read2_b32 v[28:29], v16 offset0:160 offset1:192
	v_mov_b32_e32 v16, v19
	v_pk_add_f32 v[6:7], v[6:7], v[16:17]
	s_waitcnt lgkmcnt(6)
	v_mov_b32_e32 v16, v12
	v_mov_b32_e32 v17, v10
	v_add_u32_e32 v9, 0x8e00, v5
	v_pk_add_f32 v[6:7], v[6:7], v[16:17]
	v_mov_b32_e32 v10, v13
	ds_read2_b32 v[30:31], v9 offset0:96 offset1:128
	v_add_u32_e32 v9, 0x8600, v5
	v_pk_add_f32 v[6:7], v[6:7], v[10:11]
	s_waitcnt lgkmcnt(5)
	v_mov_b32_e32 v10, v20
	v_mov_b32_e32 v11, v14
	ds_read2_b32 v[32:33], v9 offset0:96 offset1:128
	v_pk_add_f32 v[6:7], v[6:7], v[10:11]
	v_mov_b32_e32 v14, v21
	v_pk_add_f32 v[6:7], v[6:7], v[14:15]
	s_waitcnt lgkmcnt(4)
	v_mov_b32_e32 v10, v24
	v_mov_b32_e32 v11, v22
	v_pk_add_f32 v[6:7], v[6:7], v[10:11]
	v_mov_b32_e32 v22, v25
	v_pk_add_f32 v[6:7], v[6:7], v[22:23]
	s_waitcnt lgkmcnt(2)
	v_mov_b32_e32 v10, v28
	v_mov_b32_e32 v11, v26
	v_pk_add_f32 v[6:7], v[6:7], v[10:11]
	v_mov_b32_e32 v26, v29
	v_pk_add_f32 v[6:7], v[6:7], v[26:27]
	s_waitcnt lgkmcnt(0)
	v_mov_b32_e32 v10, v32
	v_mov_b32_e32 v11, v30
	v_pk_add_f32 v[6:7], v[6:7], v[10:11]
	v_mov_b32_e32 v30, v33
	v_pk_add_f32 v[6:7], v[6:7], v[30:31]
	s_mov_b32 s4, 0x3b000000
	v_pk_mul_f32 v[6:7], v[6:7], s[4:5] op_sel_hi:[1,0]
	s_mov_b32 s4, 0xf800000
	v_fma_f32 v6, -v7, v7, v6
	v_cmp_ngt_f32_e32 vcc, 0, v6
	v_add_u32_e32 v5, 0x9000, v5
	s_nop 0
	v_cndmask_b32_e32 v6, 0, v6, vcc
	v_add_f32_e32 v6, 0x3727c5ac, v6
	v_mul_f32_e32 v9, 0x4f800000, v6
	v_cmp_gt_f32_e32 vcc, s4, v6
	s_nop 1
	v_cndmask_b32_e32 v6, v6, v9, vcc
	v_sqrt_f32_e32 v9, v6
	s_nop 0
	v_add_u32_e32 v10, -1, v9
	v_fma_f32 v11, -v10, v9, v6
	v_cmp_ge_f32_e64 s[4:5], 0, v11
	v_add_u32_e32 v11, 1, v9
	s_nop 0
	v_cndmask_b32_e64 v10, v9, v10, s[4:5]
	v_fma_f32 v9, -v11, v9, v6
	v_cmp_lt_f32_e64 s[4:5], 0, v9
	s_nop 1
	v_cndmask_b32_e64 v9, v10, v11, s[4:5]
	v_mul_f32_e32 v10, 0x37800000, v9
	v_cndmask_b32_e32 v9, v9, v10, vcc
	v_mov_b32_e32 v10, 0x260
	v_cmp_class_f32_e32 vcc, v6, v10
	s_nop 1
	v_cndmask_b32_e32 v6, v9, v6, vcc
	v_div_scale_f32 v9, s[4:5], v6, v6, 1.0
	v_rcp_f32_e32 v10, v9
	s_lshl_b32 s4, s16, 12
	s_or_b32 s4, s4, s3
	v_fma_f32 v11, -v9, v10, 1.0
	v_fmac_f32_e32 v10, v11, v10
	v_div_scale_f32 v11, vcc, 1.0, v6, 1.0
	v_mul_f32_e32 v12, v11, v10
	v_fma_f32 v13, -v9, v12, v11
	v_fmac_f32_e32 v12, v13, v10
	v_fma_f32 v9, -v9, v12, v11
	v_div_fmas_f32 v9, v9, v10, v12
	v_or_b32_e32 v10, s4, v0
	v_mov_b32_e32 v11, 0
	v_lshlrev_b64 v[10:11], 2, v[10:11]
	v_div_fixup_f32 v9, v9, v6, 1.0
	v_lshl_add_u64 v[12:13], s[12:13], 0, v[10:11]
	ds_write2_b32 v5, v7, v9 offset0:32 offset1:64
	global_store_dword v[12:13], v7, off
	v_lshl_add_u64 v[6:7], s[14:15], 0, v[10:11]
	global_store_dword v[6:7], v9, off

_Z7k_scan3PKjPKfS2_S2_S2_S2_PKDF16_S4_S4_7EpiArgs:
	s_mov_b32 s24, s3
	s_ashr_i32 s25, s3, 31
	s_lshl_b32 s20, s2, 6
	s_load_dwordx8 s[4:11], s[0:1], 0x0
	s_load_dwordx8 s[12:19], s[0:1], 0x20
	s_lshl_b64 s[22:23], s[24:25], 12
	s_ashr_i32 s21, s20, 31
	s_add_u32 s22, s22, s20
	s_addc_u32 s23, s23, s21
	s_lshl_b64 s[26:27], s[22:23], 6
	s_waitcnt lgkmcnt(0)
	s_add_u32 s6, s6, s26
	s_addc_u32 s7, s7, s27
	s_add_u32 s8, s8, s26
	s_addc_u32 s9, s9, s27
	s_lshl_b32 s3, s3, 22
	s_and_b32 s26, s3, 0x400000
	v_lshlrev_b32_e32 v1, 4, v0
	s_add_u32 s3, s16, s26
	global_load_dwordx4 v[108:111], v1, s[6:7]
	global_load_dwordx4 v[114:117], v1, s[8:9]
	s_addc_u32 s8, s17, 0
	s_lshl_b64 s[6:7], s[20:21], 10
	s_add_u32 s3, s3, s6
	s_addc_u32 s16, s8, s7
	s_lshl_b32 s6, s24, 6
	s_and_b32 s8, s6, 0xffffff80
	s_ashr_i32 s9, s8, 31
	s_lshl_b64 s[6:7], s[8:9], 1
	v_mov_b32_e32 v85, 0
	s_add_u32 s6, s3, s6
	s_addc_u32 s7, s16, s7
	v_and_b32_e32 v82, 0xf0, v1
	v_mov_b32_e32 v83, v85
	v_lshlrev_b32_e32 v8, 5, v0
	v_lshl_add_u64 v[2:3], s[6:7], 0, v[82:83]
	v_lshlrev_b32_e32 v83, 6, v0
	s_movk_i32 s3, 0x3e00
	v_mov_b32_e32 v6, 0x2000
	v_and_b32_e32 v4, 0x3c00, v83
	v_mov_b32_e32 v5, v85
	v_bitop3_b32 v6, v8, s3, v6 bitop3:0xc8
	v_lshl_add_u64 v[4:5], v[2:3], 0, v[4:5]
	v_lshlrev_b32_e32 v6, 1, v6
	v_mov_b32_e32 v7, v85
	v_lshl_add_u64 v[6:7], v[2:3], 0, v[6:7]
	global_load_dwordx4 v[118:121], v[4:5], off
	global_load_dwordx4 v[122:125], v[6:7], off
	s_movk_i32 s3, 0x5e00
	v_mov_b32_e32 v4, 0x4000
	v_bitop3_b32 v4, v8, s3, v4 bitop3:0xc8
	s_movk_i32 s3, 0x7e00
	v_mov_b32_e32 v6, 0x6000
	v_lshlrev_b32_e32 v4, 1, v4
	v_mov_b32_e32 v5, v85
	v_bitop3_b32 v6, v8, s3, v6 bitop3:0xc8
	v_lshl_add_u64 v[4:5], v[2:3], 0, v[4:5]
	v_lshlrev_b32_e32 v6, 1, v6
	v_mov_b32_e32 v7, v85
	v_lshl_add_u64 v[2:3], v[2:3], 0, v[6:7]
	global_load_dwordx4 v[126:129], v[4:5], off
	global_load_dwordx4 v[130:133], v[2:3], off
	v_lshlrev_b32_e32 v9, 3, v0
	v_lshrrev_b32_e32 v107, 6, v0
	v_lshlrev_b32_e32 v2, 13, v107
	v_and_b32_e32 v3, 0x1f8, v9
	v_or_b32_e32 v2, v2, v3
	v_lshlrev_b32_e32 v86, 1, v2
	v_or_b32_e32 v2, 0x10000, v86
	global_load_dwordx4 v[78:81], v2, s[18:19]
	global_load_dwordx4 v[74:77], v2, s[18:19] offset:1024
	global_load_dwordx4 v[70:73], v2, s[18:19] offset:2048
	global_load_dwordx4 v[66:69], v2, s[18:19] offset:3072
	v_or_b32_e32 v2, 0x11000, v86
	global_load_dwordx4 v[62:65], v2, s[18:19]
	global_load_dwordx4 v[58:61], v2, s[18:19] offset:1024
	global_load_dwordx4 v[54:57], v2, s[18:19] offset:2048
	global_load_dwordx4 v[50:53], v2, s[18:19] offset:3072
	v_or_b32_e32 v2, 0x12000, v86
	global_load_dwordx4 v[46:49], v2, s[18:19]
	global_load_dwordx4 v[42:45], v2, s[18:19] offset:1024
	global_load_dwordx4 v[38:41], v2, s[18:19] offset:2048
	global_load_dwordx4 v[34:37], v2, s[18:19] offset:3072
	v_or_b32_e32 v87, 0x13000, v86
	global_load_dwordx4 v[30:33], v87, s[18:19]
	global_load_dwordx4 v[26:29], v87, s[18:19] offset:1024
	global_load_dwordx4 v[22:25], v87, s[18:19] offset:2048
	global_load_dwordx4 v[18:21], v87, s[18:19] offset:3072
	global_load_dwordx4 v[2:5], v83, s[10:11] offset:48
	global_load_dwordx4 v[6:9], v83, s[10:11] offset:32
	global_load_dwordx4 v[10:13], v83, s[10:11] offset:16
	global_load_dwordx4 v[14:17], v83, s[10:11]
	s_ashr_i32 s3, s2, 31
	s_lshl_b64 s[6:7], s[24:25], 10
	s_lshl_b64 s[10:11], s[2:3], 4
	s_add_u32 s6, s6, s10
	s_addc_u32 s7, s7, s11
	s_lshl_b64 s[6:7], s[6:7], 10
	s_add_u32 s6, s14, s6
	v_lshlrev_b32_e32 v84, 2, v0
	s_addc_u32 s7, s15, s7
	v_lshl_add_u64 v[94:95], s[6:7], 0, v[84:85]
	s_movk_i32 s3, 0x1000
	v_add_co_u32_e32 v102, vcc, s3, v94
	s_movk_i32 s16, 0x2000
	s_nop 0
	v_addc_co_u32_e32 v103, vcc, 0, v95, vcc
	v_add_co_u32_e32 v96, vcc, s16, v94
	s_movk_i32 s3, 0x3000
	s_nop 0
	v_addc_co_u32_e32 v97, vcc, 0, v95, vcc
	s_lshl_b64 s[10:11], s[22:23], 10
	v_add_co_u32_e32 v104, vcc, s3, v94
	s_add_u32 s14, s4, s10
	global_load_dword v88, v[96:97], off offset:-4096
	global_load_dword v90, v[96:97], off
	global_load_dword v91, v[96:97], off offset:1024
	global_load_dword v92, v[96:97], off offset:2048
	global_load_dword v93, v[96:97], off offset:3072
	v_addc_co_u32_e32 v105, vcc, 0, v95, vcc
	global_load_dword v94, v84, s[6:7]
	global_load_dword v89, v[102:103], off offset:1024
	global_load_dword v96, v[102:103], off offset:2048
	global_load_dword v97, v[102:103], off offset:3072
	global_load_dword v98, v[104:105], off
	global_load_dword v99, v[104:105], off offset:1024
	global_load_dword v100, v[104:105], off offset:2048
	global_load_dword v101, v[104:105], off offset:3072
	s_addc_u32 s15, s5, s11
	global_load_dword v95, v84, s[6:7] offset:1024
	global_load_dword v102, v84, s[6:7] offset:2048
	global_load_dword v103, v84, s[6:7] offset:3072
	global_load_dword v87, v84, s[12:13]
	global_load_dword v113, v84, s[14:15]
	global_load_dword v112, v84, s[14:15] offset:1024
	v_or_b32_e32 v104, 0x8800, v82
	v_lshrrev_b32_e32 v82, 4, v0
	s_movk_i32 s3, 0x110
	s_waitcnt vmcnt(44)
	ds_write_b128 v1, v[108:111] offset:52224
	s_waitcnt vmcnt(43)
	ds_write_b128 v1, v[114:117] offset:56320
	v_mad_u32_u24 v1, v82, s3, v104
	v_and_b32_e32 v109, 15, v0
	s_mov_b32 s11, 0
	v_mul_u32_u24_e32 v111, 0x110, v82
	s_mov_b32 s12, 0
	s_waitcnt vmcnt(42)
	ds_write_b128 v1, v[118:121]
	v_or_b32_e32 v1, 0x100, v0
	v_lshrrev_b32_e32 v106, 4, v1
	v_mad_u32_u24 v1, v106, s3, v104
	s_waitcnt vmcnt(41)
	ds_write_b128 v1, v[122:125]
	v_or_b32_e32 v1, 0x200, v0
	v_lshrrev_b32_e32 v83, 4, v1
	v_mad_u32_u24 v1, v83, s3, v104
	v_mul_u32_u24_e32 v110, 0x110, v106
	v_mul_u32_u24_e32 v108, 0x110, v83
	s_waitcnt vmcnt(40)
	ds_write_b128 v1, v[126:129]
	v_or_b32_e32 v1, 0x300, v0
	v_lshrrev_b32_e32 v1, 4, v1
	v_mad_u32_u24 v104, v1, s3, v104
	s_waitcnt vmcnt(39)
	ds_write_b128 v104, v[130:133]
	v_lshrrev_b32_e32 v104, 1, v0
	v_and_b32_e32 v178, 24, v104
	v_lshlrev_b32_e32 v104, 1, v178
	v_mad_u32_u24 v179, v109, s3, v104
	s_waitcnt lgkmcnt(0)
	s_barrier
	ds_read_b128 v[114:117], v179 offset:34816
	ds_read_b128 v[118:121], v179 offset:34880
	s_waitcnt vmcnt(38) lgkmcnt(1)
	v_mfma_f32_16x16x32_f16 v[122:125], v[78:81], v[114:117], 0
	ds_read_b128 v[126:129], v179 offset:34944
	ds_read_b128 v[130:133], v179 offset:35008
	s_movk_i32 s3, 0x210
	v_lshl_add_u64 v[104:105], s[14:15], 0, v[84:85]
	v_mul_u32_u24_e32 v232, 12, v0
	v_mov_b32_e32 v233, 0
	v_lshl_add_u64 v[104:105], v[104:105], 0, v[232:233]
	s_waitcnt vmcnt(34)
	v_mfma_f32_16x16x32_f16 v[134:137], v[62:65], v[114:117], 0
	v_mul_u32_u24_e32 v85, 0x110, v1
	s_waitcnt vmcnt(30)
	v_mfma_f32_16x16x32_f16 v[138:141], v[46:49], v[114:117], 0
	s_waitcnt vmcnt(26)
	v_mfma_f32_16x16x32_f16 v[114:117], v[30:33], v[114:117], 0
	s_waitcnt lgkmcnt(2)
	v_mfma_f32_16x16x32_f16 v[122:125], v[74:77], v[118:121], v[122:125]
	v_mfma_f32_16x16x32_f16 v[134:137], v[58:61], v[118:121], v[134:137]
	v_mfma_f32_16x16x32_f16 v[138:141], v[42:45], v[118:121], v[138:141]
	s_waitcnt vmcnt(25)
	v_mfma_f32_16x16x32_f16 v[114:117], v[26:29], v[118:121], v[114:117]
	s_waitcnt lgkmcnt(1)
	v_mfma_f32_16x16x32_f16 v[122:125], v[70:73], v[126:129], v[122:125]
	v_mfma_f32_16x16x32_f16 v[134:137], v[54:57], v[126:129], v[134:137]
	v_mfma_f32_16x16x32_f16 v[138:141], v[38:41], v[126:129], v[138:141]
	s_waitcnt vmcnt(24)
	v_mfma_f32_16x16x32_f16 v[114:117], v[22:25], v[126:129], v[114:117]
	s_waitcnt lgkmcnt(0)
	v_mfma_f32_16x16x32_f16 v[122:125], v[66:69], v[130:133], v[122:125]
	v_mfma_f32_16x16x32_f16 v[134:137], v[50:53], v[130:133], v[134:137]
	v_mfma_f32_16x16x32_f16 v[138:141], v[34:37], v[130:133], v[138:141]
	s_nop 5
	v_cvt_pk_f16_f32 v121, v124, v125
	v_cvt_pk_f16_f32 v120, v122, v123
	s_waitcnt vmcnt(23)
	v_lshlrev_b32_e32 v228, 4, v0
	v_add_u32_e32 v229, 0x1000, v228
	v_add_u32_e32 v230, 0x2000, v228
	v_add_u32_e32 v231, 0x3000, v228
	global_load_dwordx4 v[180:183], v228, s[14:15] nt
	global_load_dwordx4 v[184:187], v229, s[14:15] nt
	global_load_dwordx4 v[188:191], v230, s[14:15] nt
	global_load_dwordx4 v[192:195], v231, s[14:15] nt
	v_mfma_f32_16x16x32_f16 v[116:119], v[18:21], v[130:133], v[114:117]
	ds_read_b128 v[126:129], v179 offset:39168
	ds_read_b128 v[130:133], v179 offset:39232
	ds_read_b128 v[146:149], v179 offset:39296
	ds_read_b128 v[150:153], v179 offset:39360
	v_and_b32_e32 v115, 0xc0, v0
	s_waitcnt lgkmcnt(3)
	v_mfma_f32_16x16x32_f16 v[142:145], v[78:81], v[126:129], 0
	v_lshl_or_b32 v115, v115, 1, v178
	v_mad_u32_u24 v115, v109, s3, v115
	v_lshrrev_b32_e32 v114, 2, v0
	v_mfma_f32_16x16x32_f16 v[154:157], v[62:65], v[126:129], 0
	s_mov_b32 s3, 0xcc00
	v_mfma_f32_16x16x32_f16 v[158:161], v[46:49], v[126:129], 0
	v_mfma_f32_16x16x32_f16 v[126:129], v[30:33], v[126:129], 0
	s_waitcnt lgkmcnt(2)
	v_mfma_f32_16x16x32_f16 v[142:145], v[74:77], v[130:133], v[142:145]
	v_mfma_f32_16x16x32_f16 v[154:157], v[58:61], v[130:133], v[154:157]
	v_mfma_f32_16x16x32_f16 v[158:161], v[42:45], v[130:133], v[158:161]
	v_mfma_f32_16x16x32_f16 v[126:129], v[26:29], v[130:133], v[126:129]
	s_waitcnt lgkmcnt(1)
	v_mfma_f32_16x16x32_f16 v[142:145], v[70:73], v[146:149], v[142:145]
	v_mfma_f32_16x16x32_f16 v[154:157], v[54:57], v[146:149], v[154:157]
	v_mfma_f32_16x16x32_f16 v[158:161], v[38:41], v[146:149], v[158:161]
	v_mfma_f32_16x16x32_f16 v[126:129], v[22:25], v[146:149], v[126:129]
	ds_read_b128 v[130:133], v179 offset:43520
	ds_read_b128 v[146:149], v179 offset:43584
	ds_read_b128 v[162:165], v179 offset:43648
	ds_read_b128 v[166:169], v179 offset:43712
	s_load_dwordx4 s[4:7], s[0:1], 0x40
	s_nop 0
	s_load_dwordx2 s[0:1], s[0:1], 0x88
	s_waitcnt lgkmcnt(0)
	v_mfma_f32_16x16x32_f16 v[142:145], v[66:69], v[150:153], v[142:145]
	v_mfma_f32_16x16x32_f16 v[154:157], v[50:53], v[150:153], v[154:157]
	v_mfma_f32_16x16x32_f16 v[158:161], v[34:37], v[150:153], v[158:161]
	v_mfma_f32_16x16x32_f16 v[126:129], v[18:21], v[150:153], v[126:129]
	v_mfma_f32_16x16x32_f16 v[150:153], v[78:81], v[130:133], 0
	v_mfma_f32_16x16x32_f16 v[170:173], v[62:65], v[130:133], 0
	v_mfma_f32_16x16x32_f16 v[174:177], v[46:49], v[130:133], 0
	v_mfma_f32_16x16x32_f16 v[130:133], v[30:33], v[130:133], 0
	v_mfma_f32_16x16x32_f16 v[150:153], v[74:77], v[146:149], v[150:153]
	v_mfma_f32_16x16x32_f16 v[170:173], v[58:61], v[146:149], v[170:173]
	v_mfma_f32_16x16x32_f16 v[174:177], v[42:45], v[146:149], v[174:177]
	v_mfma_f32_16x16x32_f16 v[130:133], v[26:29], v[146:149], v[130:133]
	ds_read_b128 v[146:149], v179 offset:47872
	v_mfma_f32_16x16x32_f16 v[150:153], v[70:73], v[162:165], v[150:153]
	v_mfma_f32_16x16x32_f16 v[170:173], v[54:57], v[162:165], v[170:173]
	v_mfma_f32_16x16x32_f16 v[174:177], v[38:41], v[162:165], v[174:177]
	v_mfma_f32_16x16x32_f16 v[130:133], v[22:25], v[162:165], v[130:133]
	ds_read_b128 v[162:165], v179 offset:47936
	s_waitcnt lgkmcnt(1)
	v_mfma_f32_16x16x32_f16 v[78:81], v[78:81], v[146:149], 0
	v_mfma_f32_16x16x32_f16 v[62:65], v[62:65], v[146:149], 0
	v_mfma_f32_16x16x32_f16 v[46:49], v[46:49], v[146:149], 0
	v_mfma_f32_16x16x32_f16 v[30:33], v[30:33], v[146:149], 0
	v_mfma_f32_16x16x32_f16 v[150:153], v[66:69], v[166:169], v[150:153]
	v_mfma_f32_16x16x32_f16 v[170:173], v[50:53], v[166:169], v[170:173]
	v_mfma_f32_16x16x32_f16 v[174:177], v[34:37], v[166:169], v[174:177]
	v_mfma_f32_16x16x32_f16 v[130:133], v[18:21], v[166:169], v[130:133]
	ds_read_b128 v[166:169], v179 offset:48000
	s_waitcnt lgkmcnt(1)
	v_mfma_f32_16x16x32_f16 v[74:77], v[74:77], v[162:165], v[78:81]
	v_mfma_f32_16x16x32_f16 v[58:61], v[58:61], v[162:165], v[62:65]
	s_nop 1
	ds_read_b128 v[78:81], v179 offset:48064
	v_mfma_f32_16x16x32_f16 v[42:45], v[42:45], v[162:165], v[46:49]
	v_cvt_pk_f16_f32 v63, v144, v145
	v_cvt_pk_f16_f32 v62, v142, v143
	v_cvt_pk_f16_f32 v65, v156, v157
	v_mfma_f32_16x16x32_f16 v[26:29], v[26:29], v[162:165], v[30:33]
	v_cvt_pk_f16_f32 v64, v154, v155
	v_cvt_pk_f16_f32 v47, v172, v173
	v_cvt_pk_f16_f32 v46, v170, v171
	s_waitcnt lgkmcnt(1)
	v_mfma_f32_16x16x32_f16 v[70:73], v[70:73], v[166:169], v[74:77]
	v_add_u32_e32 v32, 0x6000, v115
	v_mfma_f32_16x16x32_f16 v[54:57], v[54:57], v[166:169], v[58:61]
	s_nop 0
	v_cvt_pk_f16_f32 v75, v136, v137
	v_cvt_pk_f16_f32 v74, v134, v135
	ds_write2_b64 v115, v[120:121], v[74:75] offset1:4
	v_mfma_f32_16x16x32_f16 v[38:41], v[38:41], v[166:169], v[42:45]
	v_add_u32_e32 v58, 0x2000, v115
	ds_write2_b64 v58, v[62:63], v[64:65] offset0:32 offset1:36
	v_mfma_f32_16x16x32_f16 v[22:25], v[22:25], v[166:169], v[26:29]
	v_add_u32_e32 v44, 0x4000, v115
	v_cvt_pk_f16_f32 v43, v176, v177
	v_cvt_pk_f16_f32 v42, v174, v175
	s_waitcnt lgkmcnt(2)
	v_mfma_f32_16x16x32_f16 v[66:69], v[66:69], v[78:81], v[70:73]
	v_mfma_f32_16x16x32_f16 v[50:53], v[50:53], v[78:81], v[54:57]
	s_nop 1
	v_cvt_pk_f16_f32 v71, v140, v141
	v_cvt_pk_f16_f32 v70, v138, v139
	v_cvt_pk_f16_f32 v73, v118, v119
	v_mfma_f32_16x16x32_f16 v[34:37], v[34:37], v[78:81], v[38:41]
	v_cvt_pk_f16_f32 v55, v160, v161
	v_cvt_pk_f16_f32 v54, v158, v159
	v_cvt_pk_f16_f32 v57, v128, v129
	v_mfma_f32_16x16x32_f16 v[18:21], v[18:21], v[78:81], v[22:25]
	v_cvt_pk_f16_f32 v56, v126, v127
	v_cvt_pk_f16_f32 v39, v132, v133
	v_cvt_pk_f16_f32 v38, v130, v131
	v_cvt_pk_f16_f32 v72, v116, v117
	ds_write2_b64 v58, v[54:55], v[56:57] offset0:40 offset1:44
	v_cvt_pk_f16_f32 v55, v152, v153
	v_cvt_pk_f16_f32 v54, v150, v151
	ds_write2_b64 v44, v[42:43], v[38:39] offset0:72 offset1:76
	v_cvt_pk_f16_f32 v39, v68, v69
	v_cvt_pk_f16_f32 v38, v66, v67
	v_cvt_pk_f16_f32 v31, v52, v53
	v_cvt_pk_f16_f32 v30, v50, v51
	v_cvt_pk_f16_f32 v27, v36, v37
	v_cvt_pk_f16_f32 v26, v34, v35
	v_cvt_pk_f16_f32 v21, v20, v21
	v_cvt_pk_f16_f32 v20, v18, v19
	v_lshlrev_b32_e32 v19, 1, v0
	ds_write2_b64 v115, v[70:71], v[72:73] offset0:8 offset1:12
	ds_write2_b64 v44, v[54:55], v[46:47] offset0:64 offset1:68
	ds_write2_b64 v32, v[38:39], v[30:31] offset0:96 offset1:100
	ds_write2_b64 v32, v[26:27], v[20:21] offset0:104 offset1:108
	s_waitcnt lgkmcnt(0)
	s_barrier
	v_mov_b32_e32 v57, 0xcc00
	ds_read_b128 v[116:119], v57 offset:0
	ds_read_b128 v[120:123], v57 offset:16
	ds_read_b128 v[124:127], v57 offset:32
	ds_read_b128 v[128:131], v57 offset:48
	ds_read_b128 v[132:135], v57 offset:4096
	ds_read_b128 v[136:139], v57 offset:4112
	ds_read_b128 v[140:143], v57 offset:4128
	ds_read_b128 v[144:147], v57 offset:4144
	ds_read_u16 v52, v19
	s_mov_b32 s10, 0x5000
	s_mov_b32 s11, 0
	v_lshl_add_u64 v[58:59], v[104:105], 0, s[10:11]
	s_mov_b32 s10, 0x2000
	v_lshl_add_u64 v[50:51], v[58:59], 0, s[10:11]
	s_mov_b32 s10, 0x4000
	s_waitcnt vmcnt(3)
	v_cvt_f32_f16_e32 v46, v180
	v_fma_mix_f32 v44, v180, v180, 0 op_sel:[0,1,0] op_sel_hi:[1,1,0]
	v_pk_mul_f32 v[20:21], v[46:47], v[14:15] op_sel_hi:[0,1]
	v_pk_mul_f32 v[22:23], v[46:47], v[16:17] op_sel_hi:[0,1]
	v_pk_mul_f32 v[24:25], v[46:47], v[10:11] op_sel_hi:[0,1]
	v_pk_mul_f32 v[26:27], v[46:47], v[12:13] op_sel_hi:[0,1]
	v_pk_mul_f32 v[28:29], v[46:47], v[6:7] op_sel_hi:[0,1]
	v_pk_mul_f32 v[30:31], v[46:47], v[8:9] op_sel_hi:[0,1]
	v_pk_mul_f32 v[32:33], v[46:47], v[2:3] op_sel_hi:[0,1]
	v_pk_mul_f32 v[34:35], v[46:47], v[4:5] op_sel_hi:[0,1]
	v_exp_f32_e32 v20, v20
	v_exp_f32_e32 v21, v21
	v_exp_f32_e32 v22, v22
	v_exp_f32_e32 v23, v23
	v_exp_f32_e32 v24, v24
	v_exp_f32_e32 v25, v25
	v_exp_f32_e32 v26, v26
	v_exp_f32_e32 v27, v27
	v_exp_f32_e32 v28, v28
	v_exp_f32_e32 v29, v29
	v_exp_f32_e32 v30, v30
	v_exp_f32_e32 v31, v31
	v_exp_f32_e32 v32, v32
	v_exp_f32_e32 v33, v33
	v_exp_f32_e32 v34, v34
	v_exp_f32_e32 v35, v35
	s_mov_b32 s12, 0
.Lsc3_loop:
	s_waitcnt lgkmcnt(0)
	ds_read_b128 v[196:199], v57 offset:64
	ds_read_b128 v[200:203], v57 offset:80
	ds_read_b128 v[204:207], v57 offset:96
	ds_read_b128 v[208:211], v57 offset:112
	ds_read_b128 v[212:215], v57 offset:4160
	ds_read_b128 v[216:219], v57 offset:4176
	ds_read_b128 v[220:223], v57 offset:4192
	ds_read_b128 v[224:227], v57 offset:4208
	v_cvt_f32_f16_e32 v46, v181
	v_cvt_f32_f16_e32 v53, v52
	ds_read_u16 v52, v19 offset:528
	v_pk_mul_f32 v[94:95], v[94:95], v[20:21]
	v_pk_mul_f32 v[20:21], v[46:47], v[14:15] op_sel_hi:[0,1]
	v_mul_f32_e32 v55, 0xbfb8aa3b, v53
	v_pk_mul_f32 v[102:103], v[102:103], v[22:23]
	v_exp_f32_e32 v20, v20
	v_pk_mul_f32 v[22:23], v[46:47], v[16:17] op_sel_hi:[0,1]
	v_pk_fma_f32 v[94:95], v[44:45], v[116:117], v[94:95] op_sel_hi:[0,1,1]
	v_exp_f32_e32 v21, v21
	v_pk_mul_f32 v[48:49], v[94:95], v[132:133]
	v_pk_mul_f32 v[88:89], v[88:89], v[24:25]
	v_exp_f32_e32 v22, v22
	v_pk_mul_f32 v[24:25], v[46:47], v[10:11] op_sel_hi:[0,1]
	v_pk_fma_f32 v[102:103], v[44:45], v[118:119], v[102:103] op_sel_hi:[0,1,1]
	v_exp_f32_e32 v23, v23
	v_pk_fma_f32 v[48:49], v[102:103], v[134:135], v[48:49]
	v_exp_f32_e32 v55, v55
	v_pk_mul_f32 v[96:97], v[96:97], v[26:27]
	v_exp_f32_e32 v24, v24
	v_pk_mul_f32 v[26:27], v[46:47], v[12:13] op_sel_hi:[0,1]
	v_pk_fma_f32 v[88:89], v[44:45], v[120:121], v[88:89] op_sel_hi:[0,1,1]
	v_exp_f32_e32 v25, v25
	v_pk_fma_f32 v[48:49], v[88:89], v[136:137], v[48:49]
	v_pk_mul_f32 v[90:91], v[90:91], v[28:29]
	v_exp_f32_e32 v26, v26
	v_pk_mul_f32 v[28:29], v[46:47], v[6:7] op_sel_hi:[0,1]
	v_pk_fma_f32 v[96:97], v[44:45], v[122:123], v[96:97] op_sel_hi:[0,1,1]
	v_exp_f32_e32 v27, v27
	v_pk_fma_f32 v[48:49], v[96:97], v[138:139], v[48:49]
	v_add_f32_e32 v55, 1.0, v55
	v_pk_mul_f32 v[92:93], v[92:93], v[30:31]
	v_exp_f32_e32 v28, v28
	v_pk_mul_f32 v[30:31], v[46:47], v[8:9] op_sel_hi:[0,1]
	v_pk_fma_f32 v[90:91], v[44:45], v[124:125], v[90:91] op_sel_hi:[0,1,1]
	v_exp_f32_e32 v29, v29
	v_pk_fma_f32 v[48:49], v[90:91], v[140:141], v[48:49]
	v_pk_mul_f32 v[98:99], v[98:99], v[32:33]
	v_exp_f32_e32 v30, v30
	v_pk_mul_f32 v[32:33], v[46:47], v[2:3] op_sel_hi:[0,1]
	v_pk_fma_f32 v[92:93], v[44:45], v[126:127], v[92:93] op_sel_hi:[0,1,1]
	v_exp_f32_e32 v31, v31
	v_pk_fma_f32 v[48:49], v[92:93], v[142:143], v[48:49]
	v_rcp_f32_e32 v55, v55
	v_pk_mul_f32 v[100:101], v[100:101], v[34:35]
	v_exp_f32_e32 v32, v32
	v_pk_mul_f32 v[34:35], v[46:47], v[4:5] op_sel_hi:[0,1]
	v_pk_fma_f32 v[98:99], v[44:45], v[128:129], v[98:99] op_sel_hi:[0,1,1]
	v_exp_f32_e32 v33, v33
	v_pk_fma_f32 v[48:49], v[98:99], v[144:145], v[48:49]
	v_exp_f32_e32 v34, v34
	v_pk_fma_f32 v[100:101], v[44:45], v[130:131], v[100:101] op_sel_hi:[0,1,1]
	v_exp_f32_e32 v35, v35
	v_pk_fma_f32 v[48:49], v[100:101], v[146:147], v[48:49]
	v_add_f32_e32 v54, v48, v49
	v_fma_mix_f32 v54, v87, v180, v54 op_sel:[0,1,0] op_sel_hi:[0,1,0]
	v_mul_f32_e32 v54, v54, v53
	v_fma_mix_f32 v44, v181, v181, 0 op_sel:[0,1,0] op_sel_hi:[1,1,0]
	v_fma_mixlo_f16 v56, v54, v55, 0
	ds_write_b16 v19, v56
	v_add_u32_e32 v19, 0x210, v19
	s_waitcnt lgkmcnt(1)
	ds_read_b128 v[116:119], v57 offset:128
	ds_read_b128 v[120:123], v57 offset:144
	ds_read_b128 v[124:127], v57 offset:160
	ds_read_b128 v[128:131], v57 offset:176
	ds_read_b128 v[132:135], v57 offset:4224
	ds_read_b128 v[136:139], v57 offset:4240
	ds_read_b128 v[140:143], v57 offset:4256
	ds_read_b128 v[144:147], v57 offset:4272
	v_cvt_f32_f16_e32 v46, v182
	v_cvt_f32_f16_e32 v53, v52
	ds_read_u16 v52, v19 offset:528
	v_pk_mul_f32 v[94:95], v[94:95], v[20:21]
	v_pk_mul_f32 v[20:21], v[46:47], v[14:15] op_sel_hi:[0,1]
	v_mul_f32_e32 v55, 0xbfb8aa3b, v53
	v_pk_mul_f32 v[102:103], v[102:103], v[22:23]
	v_exp_f32_e32 v20, v20
	v_pk_mul_f32 v[22:23], v[46:47], v[16:17] op_sel_hi:[0,1]
	v_pk_fma_f32 v[94:95], v[44:45], v[196:197], v[94:95] op_sel_hi:[0,1,1]
	v_exp_f32_e32 v21, v21
	v_pk_mul_f32 v[48:49], v[94:95], v[212:213]
	v_pk_mul_f32 v[88:89], v[88:89], v[24:25]
	v_exp_f32_e32 v22, v22
	v_pk_mul_f32 v[24:25], v[46:47], v[10:11] op_sel_hi:[0,1]
	v_pk_fma_f32 v[102:103], v[44:45], v[198:199], v[102:103] op_sel_hi:[0,1,1]
	v_exp_f32_e32 v23, v23
	v_pk_fma_f32 v[48:49], v[102:103], v[214:215], v[48:49]
	v_exp_f32_e32 v55, v55
	v_pk_mul_f32 v[96:97], v[96:97], v[26:27]
	v_exp_f32_e32 v24, v24
	v_pk_mul_f32 v[26:27], v[46:47], v[12:13] op_sel_hi:[0,1]
	v_pk_fma_f32 v[88:89], v[44:45], v[200:201], v[88:89] op_sel_hi:[0,1,1]
	v_exp_f32_e32 v25, v25
	v_pk_fma_f32 v[48:49], v[88:89], v[216:217], v[48:49]
	v_pk_mul_f32 v[90:91], v[90:91], v[28:29]
	v_exp_f32_e32 v26, v26
	v_pk_mul_f32 v[28:29], v[46:47], v[6:7] op_sel_hi:[0,1]
	v_pk_fma_f32 v[96:97], v[44:45], v[202:203], v[96:97] op_sel_hi:[0,1,1]
	v_exp_f32_e32 v27, v27
	v_pk_fma_f32 v[48:49], v[96:97], v[218:219], v[48:49]
	v_add_f32_e32 v55, 1.0, v55
	v_pk_mul_f32 v[92:93], v[92:93], v[30:31]
	v_exp_f32_e32 v28, v28
	v_pk_mul_f32 v[30:31], v[46:47], v[8:9] op_sel_hi:[0,1]
	v_pk_fma_f32 v[90:91], v[44:45], v[204:205], v[90:91] op_sel_hi:[0,1,1]
	v_exp_f32_e32 v29, v29
	v_pk_fma_f32 v[48:49], v[90:91], v[220:221], v[48:49]
	v_pk_mul_f32 v[98:99], v[98:99], v[32:33]
	v_exp_f32_e32 v30, v30
	v_pk_mul_f32 v[32:33], v[46:47], v[2:3] op_sel_hi:[0,1]
	v_pk_fma_f32 v[92:93], v[44:45], v[206:207], v[92:93] op_sel_hi:[0,1,1]
	v_exp_f32_e32 v31, v31
	v_pk_fma_f32 v[48:49], v[92:93], v[222:223], v[48:49]
	v_rcp_f32_e32 v55, v55
	v_pk_mul_f32 v[100:101], v[100:101], v[34:35]
	v_exp_f32_e32 v32, v32
	v_pk_mul_f32 v[34:35], v[46:47], v[4:5] op_sel_hi:[0,1]
	v_pk_fma_f32 v[98:99], v[44:45], v[208:209], v[98:99] op_sel_hi:[0,1,1]
	v_exp_f32_e32 v33, v33
	v_pk_fma_f32 v[48:49], v[98:99], v[224:225], v[48:49]
	v_exp_f32_e32 v34, v34
	v_pk_fma_f32 v[100:101], v[44:45], v[210:211], v[100:101] op_sel_hi:[0,1,1]
	v_exp_f32_e32 v35, v35
	v_pk_fma_f32 v[48:49], v[100:101], v[226:227], v[48:49]
	v_add_f32_e32 v54, v48, v49
	v_fma_mix_f32 v54, v87, v181, v54 op_sel:[0,1,0] op_sel_hi:[0,1,0]
	v_mul_f32_e32 v54, v54, v53
	v_fma_mix_f32 v44, v182, v182, 0 op_sel:[0,1,0] op_sel_hi:[1,1,0]
	v_fma_mixlo_f16 v56, v54, v55, 0
	ds_write_b16 v19, v56
	v_add_u32_e32 v19, 0x210, v19
	s_waitcnt lgkmcnt(1)
	ds_read_b128 v[196:199], v57 offset:192
	ds_read_b128 v[200:203], v57 offset:208
	ds_read_b128 v[204:207], v57 offset:224
	ds_read_b128 v[208:211], v57 offset:240
	ds_read_b128 v[212:215], v57 offset:4288
	ds_read_b128 v[216:219], v57 offset:4304
	ds_read_b128 v[220:223], v57 offset:4320
	ds_read_b128 v[224:227], v57 offset:4336
	v_cvt_f32_f16_e32 v46, v183
	v_cvt_f32_f16_e32 v53, v52
	ds_read_u16 v52, v19 offset:528
	v_pk_mul_f32 v[94:95], v[94:95], v[20:21]
	v_pk_mul_f32 v[20:21], v[46:47], v[14:15] op_sel_hi:[0,1]
	v_mul_f32_e32 v55, 0xbfb8aa3b, v53
	v_pk_mul_f32 v[102:103], v[102:103], v[22:23]
	v_exp_f32_e32 v20, v20
	v_pk_mul_f32 v[22:23], v[46:47], v[16:17] op_sel_hi:[0,1]
	v_pk_fma_f32 v[94:95], v[44:45], v[116:117], v[94:95] op_sel_hi:[0,1,1]
	v_exp_f32_e32 v21, v21
	v_pk_mul_f32 v[48:49], v[94:95], v[132:133]
	v_pk_mul_f32 v[88:89], v[88:89], v[24:25]
	v_exp_f32_e32 v22, v22
	v_pk_mul_f32 v[24:25], v[46:47], v[10:11] op_sel_hi:[0,1]
	v_pk_fma_f32 v[102:103], v[44:45], v[118:119], v[102:103] op_sel_hi:[0,1,1]
	v_exp_f32_e32 v23, v23
	v_pk_fma_f32 v[48:49], v[102:103], v[134:135], v[48:49]
	v_exp_f32_e32 v55, v55
	v_pk_mul_f32 v[96:97], v[96:97], v[26:27]
	v_exp_f32_e32 v24, v24
	v_pk_mul_f32 v[26:27], v[46:47], v[12:13] op_sel_hi:[0,1]
	v_pk_fma_f32 v[88:89], v[44:45], v[120:121], v[88:89] op_sel_hi:[0,1,1]
	v_exp_f32_e32 v25, v25
	v_pk_fma_f32 v[48:49], v[88:89], v[136:137], v[48:49]
	v_pk_mul_f32 v[90:91], v[90:91], v[28:29]
	v_exp_f32_e32 v26, v26
	v_pk_mul_f32 v[28:29], v[46:47], v[6:7] op_sel_hi:[0,1]
	v_pk_fma_f32 v[96:97], v[44:45], v[122:123], v[96:97] op_sel_hi:[0,1,1]
	v_exp_f32_e32 v27, v27
	v_pk_fma_f32 v[48:49], v[96:97], v[138:139], v[48:49]
	v_add_f32_e32 v55, 1.0, v55
	v_pk_mul_f32 v[92:93], v[92:93], v[30:31]
	v_exp_f32_e32 v28, v28
	v_pk_mul_f32 v[30:31], v[46:47], v[8:9] op_sel_hi:[0,1]
	v_pk_fma_f32 v[90:91], v[44:45], v[124:125], v[90:91] op_sel_hi:[0,1,1]
	v_exp_f32_e32 v29, v29
	v_pk_fma_f32 v[48:49], v[90:91], v[140:141], v[48:49]
	v_pk_mul_f32 v[98:99], v[98:99], v[32:33]
	v_exp_f32_e32 v30, v30
	v_pk_mul_f32 v[32:33], v[46:47], v[2:3] op_sel_hi:[0,1]
	v_pk_fma_f32 v[92:93], v[44:45], v[126:127], v[92:93] op_sel_hi:[0,1,1]
	v_exp_f32_e32 v31, v31
	v_pk_fma_f32 v[48:49], v[92:93], v[142:143], v[48:49]
	v_rcp_f32_e32 v55, v55
	v_pk_mul_f32 v[100:101], v[100:101], v[34:35]
	v_exp_f32_e32 v32, v32
	v_pk_mul_f32 v[34:35], v[46:47], v[4:5] op_sel_hi:[0,1]
	v_pk_fma_f32 v[98:99], v[44:45], v[128:129], v[98:99] op_sel_hi:[0,1,1]
	v_exp_f32_e32 v33, v33
	v_pk_fma_f32 v[48:49], v[98:99], v[144:145], v[48:49]
	v_exp_f32_e32 v34, v34
	v_pk_fma_f32 v[100:101], v[44:45], v[130:131], v[100:101] op_sel_hi:[0,1,1]
	v_exp_f32_e32 v35, v35
	v_pk_fma_f32 v[48:49], v[100:101], v[146:147], v[48:49]
	v_add_f32_e32 v54, v48, v49
	v_fma_mix_f32 v54, v87, v182, v54 op_sel:[0,1,0] op_sel_hi:[0,1,0]
	v_mul_f32_e32 v54, v54, v53
	v_fma_mix_f32 v44, v183, v183, 0 op_sel:[0,1,0] op_sel_hi:[1,1,0]
	v_fma_mixlo_f16 v56, v54, v55, 0
	ds_write_b16 v19, v56
	v_add_u32_e32 v19, 0x210, v19
	s_waitcnt lgkmcnt(1)
	ds_read_b128 v[116:119], v57 offset:256
	ds_read_b128 v[120:123], v57 offset:272
	ds_read_b128 v[124:127], v57 offset:288
	ds_read_b128 v[128:131], v57 offset:304
	ds_read_b128 v[132:135], v57 offset:4352
	ds_read_b128 v[136:139], v57 offset:4368
	ds_read_b128 v[140:143], v57 offset:4384
	ds_read_b128 v[144:147], v57 offset:4400
	s_waitcnt vmcnt(2)
	v_cvt_f32_f16_e32 v46, v184
	v_cvt_f32_f16_e32 v53, v52
	ds_read_u16 v52, v19 offset:528
	v_pk_mul_f32 v[94:95], v[94:95], v[20:21]
	v_pk_mul_f32 v[20:21], v[46:47], v[14:15] op_sel_hi:[0,1]
	v_mul_f32_e32 v55, 0xbfb8aa3b, v53
	v_pk_mul_f32 v[102:103], v[102:103], v[22:23]
	v_exp_f32_e32 v20, v20
	v_pk_mul_f32 v[22:23], v[46:47], v[16:17] op_sel_hi:[0,1]
	v_pk_fma_f32 v[94:95], v[44:45], v[196:197], v[94:95] op_sel_hi:[0,1,1]
	v_exp_f32_e32 v21, v21
	v_pk_mul_f32 v[48:49], v[94:95], v[212:213]
	v_pk_mul_f32 v[88:89], v[88:89], v[24:25]
	v_exp_f32_e32 v22, v22
	v_pk_mul_f32 v[24:25], v[46:47], v[10:11] op_sel_hi:[0,1]
	v_pk_fma_f32 v[102:103], v[44:45], v[198:199], v[102:103] op_sel_hi:[0,1,1]
	v_exp_f32_e32 v23, v23
	v_pk_fma_f32 v[48:49], v[102:103], v[214:215], v[48:49]
	v_exp_f32_e32 v55, v55
	v_pk_mul_f32 v[96:97], v[96:97], v[26:27]
	v_exp_f32_e32 v24, v24
	v_pk_mul_f32 v[26:27], v[46:47], v[12:13] op_sel_hi:[0,1]
	v_pk_fma_f32 v[88:89], v[44:45], v[200:201], v[88:89] op_sel_hi:[0,1,1]
	v_exp_f32_e32 v25, v25
	v_pk_fma_f32 v[48:49], v[88:89], v[216:217], v[48:49]
	v_pk_mul_f32 v[90:91], v[90:91], v[28:29]
	v_exp_f32_e32 v26, v26
	v_pk_mul_f32 v[28:29], v[46:47], v[6:7] op_sel_hi:[0,1]
	v_pk_fma_f32 v[96:97], v[44:45], v[202:203], v[96:97] op_sel_hi:[0,1,1]
	v_exp_f32_e32 v27, v27
	v_pk_fma_f32 v[48:49], v[96:97], v[218:219], v[48:49]
	v_add_f32_e32 v55, 1.0, v55
	v_pk_mul_f32 v[92:93], v[92:93], v[30:31]
	v_exp_f32_e32 v28, v28
	v_pk_mul_f32 v[30:31], v[46:47], v[8:9] op_sel_hi:[0,1]
	v_pk_fma_f32 v[90:91], v[44:45], v[204:205], v[90:91] op_sel_hi:[0,1,1]
	v_exp_f32_e32 v29, v29
	v_pk_fma_f32 v[48:49], v[90:91], v[220:221], v[48:49]
	v_pk_mul_f32 v[98:99], v[98:99], v[32:33]
	v_exp_f32_e32 v30, v30
	v_pk_mul_f32 v[32:33], v[46:47], v[2:3] op_sel_hi:[0,1]
	v_pk_fma_f32 v[92:93], v[44:45], v[206:207], v[92:93] op_sel_hi:[0,1,1]
	v_exp_f32_e32 v31, v31
	v_pk_fma_f32 v[48:49], v[92:93], v[222:223], v[48:49]
	v_rcp_f32_e32 v55, v55
	v_pk_mul_f32 v[100:101], v[100:101], v[34:35]
	v_exp_f32_e32 v32, v32
	v_pk_mul_f32 v[34:35], v[46:47], v[4:5] op_sel_hi:[0,1]
	v_pk_fma_f32 v[98:99], v[44:45], v[208:209], v[98:99] op_sel_hi:[0,1,1]
	v_exp_f32_e32 v33, v33
	v_pk_fma_f32 v[48:49], v[98:99], v[224:225], v[48:49]
	v_exp_f32_e32 v34, v34
	v_pk_fma_f32 v[100:101], v[44:45], v[210:211], v[100:101] op_sel_hi:[0,1,1]
	v_exp_f32_e32 v35, v35
	v_pk_fma_f32 v[48:49], v[100:101], v[226:227], v[48:49]
	v_add_f32_e32 v54, v48, v49
	v_fma_mix_f32 v54, v87, v183, v54 op_sel:[0,1,0] op_sel_hi:[0,1,0]
	v_mul_f32_e32 v54, v54, v53
	v_fma_mix_f32 v44, v184, v184, 0 op_sel:[0,1,0] op_sel_hi:[1,1,0]
	global_load_dwordx4 v[180:183], v[58:59], off offset:-4096 nt
	v_fma_mixlo_f16 v56, v54, v55, 0
	ds_write_b16 v19, v56
	v_add_u32_e32 v19, 0x210, v19
	s_waitcnt lgkmcnt(1)
	ds_read_b128 v[196:199], v57 offset:320
	ds_read_b128 v[200:203], v57 offset:336
	ds_read_b128 v[204:207], v57 offset:352
	ds_read_b128 v[208:211], v57 offset:368
	ds_read_b128 v[212:215], v57 offset:4416
	ds_read_b128 v[216:219], v57 offset:4432
	ds_read_b128 v[220:223], v57 offset:4448
	ds_read_b128 v[224:227], v57 offset:4464
	v_cvt_f32_f16_e32 v46, v185
	v_cvt_f32_f16_e32 v53, v52
	ds_read_u16 v52, v19 offset:528
	v_pk_mul_f32 v[94:95], v[94:95], v[20:21]
	v_pk_mul_f32 v[20:21], v[46:47], v[14:15] op_sel_hi:[0,1]
	v_mul_f32_e32 v55, 0xbfb8aa3b, v53
	v_pk_mul_f32 v[102:103], v[102:103], v[22:23]
	v_exp_f32_e32 v20, v20
	v_pk_mul_f32 v[22:23], v[46:47], v[16:17] op_sel_hi:[0,1]
	v_pk_fma_f32 v[94:95], v[44:45], v[116:117], v[94:95] op_sel_hi:[0,1,1]
	v_exp_f32_e32 v21, v21
	v_pk_mul_f32 v[48:49], v[94:95], v[132:133]
	v_pk_mul_f32 v[88:89], v[88:89], v[24:25]
	v_exp_f32_e32 v22, v22
	v_pk_mul_f32 v[24:25], v[46:47], v[10:11] op_sel_hi:[0,1]
	v_pk_fma_f32 v[102:103], v[44:45], v[118:119], v[102:103] op_sel_hi:[0,1,1]
	v_exp_f32_e32 v23, v23
	v_pk_fma_f32 v[48:49], v[102:103], v[134:135], v[48:49]
	v_exp_f32_e32 v55, v55
	v_pk_mul_f32 v[96:97], v[96:97], v[26:27]
	v_exp_f32_e32 v24, v24
	v_pk_mul_f32 v[26:27], v[46:47], v[12:13] op_sel_hi:[0,1]
	v_pk_fma_f32 v[88:89], v[44:45], v[120:121], v[88:89] op_sel_hi:[0,1,1]
	v_exp_f32_e32 v25, v25
	v_pk_fma_f32 v[48:49], v[88:89], v[136:137], v[48:49]
	v_pk_mul_f32 v[90:91], v[90:91], v[28:29]
	v_exp_f32_e32 v26, v26
	v_pk_mul_f32 v[28:29], v[46:47], v[6:7] op_sel_hi:[0,1]
	v_pk_fma_f32 v[96:97], v[44:45], v[122:123], v[96:97] op_sel_hi:[0,1,1]
	v_exp_f32_e32 v27, v27
	v_pk_fma_f32 v[48:49], v[96:97], v[138:139], v[48:49]
	v_add_f32_e32 v55, 1.0, v55
	v_pk_mul_f32 v[92:93], v[92:93], v[30:31]
	v_exp_f32_e32 v28, v28
	v_pk_mul_f32 v[30:31], v[46:47], v[8:9] op_sel_hi:[0,1]
	v_pk_fma_f32 v[90:91], v[44:45], v[124:125], v[90:91] op_sel_hi:[0,1,1]
	v_exp_f32_e32 v29, v29
	v_pk_fma_f32 v[48:49], v[90:91], v[140:141], v[48:49]
	v_pk_mul_f32 v[98:99], v[98:99], v[32:33]
	v_exp_f32_e32 v30, v30
	v_pk_mul_f32 v[32:33], v[46:47], v[2:3] op_sel_hi:[0,1]
	v_pk_fma_f32 v[92:93], v[44:45], v[126:127], v[92:93] op_sel_hi:[0,1,1]
	v_exp_f32_e32 v31, v31
	v_pk_fma_f32 v[48:49], v[92:93], v[142:143], v[48:49]
	v_rcp_f32_e32 v55, v55
	v_pk_mul_f32 v[100:101], v[100:101], v[34:35]
	v_exp_f32_e32 v32, v32
	v_pk_mul_f32 v[34:35], v[46:47], v[4:5] op_sel_hi:[0,1]
	v_pk_fma_f32 v[98:99], v[44:45], v[128:129], v[98:99] op_sel_hi:[0,1,1]
	v_exp_f32_e32 v33, v33
	v_pk_fma_f32 v[48:49], v[98:99], v[144:145], v[48:49]
	v_exp_f32_e32 v34, v34
	v_pk_fma_f32 v[100:101], v[44:45], v[130:131], v[100:101] op_sel_hi:[0,1,1]
	v_exp_f32_e32 v35, v35
	v_pk_fma_f32 v[48:49], v[100:101], v[146:147], v[48:49]
	v_add_f32_e32 v54, v48, v49
	v_fma_mix_f32 v54, v87, v184, v54 op_sel:[0,1,0] op_sel_hi:[0,1,0]
	v_mul_f32_e32 v54, v54, v53
	v_fma_mix_f32 v44, v185, v185, 0 op_sel:[0,1,0] op_sel_hi:[1,1,0]
	v_fma_mixlo_f16 v56, v54, v55, 0
	ds_write_b16 v19, v56
	v_add_u32_e32 v19, 0x210, v19
	s_waitcnt lgkmcnt(1)
	ds_read_b128 v[116:119], v57 offset:384
	ds_read_b128 v[120:123], v57 offset:400
	ds_read_b128 v[124:127], v57 offset:416
	ds_read_b128 v[128:131], v57 offset:432
	ds_read_b128 v[132:135], v57 offset:4480
	ds_read_b128 v[136:139], v57 offset:4496
	ds_read_b128 v[140:143], v57 offset:4512
	ds_read_b128 v[144:147], v57 offset:4528
	v_cvt_f32_f16_e32 v46, v186
	v_cvt_f32_f16_e32 v53, v52
	ds_read_u16 v52, v19 offset:528
	v_pk_mul_f32 v[94:95], v[94:95], v[20:21]
	v_pk_mul_f32 v[20:21], v[46:47], v[14:15] op_sel_hi:[0,1]
	v_mul_f32_e32 v55, 0xbfb8aa3b, v53
	v_pk_mul_f32 v[102:103], v[102:103], v[22:23]
	v_exp_f32_e32 v20, v20
	v_pk_mul_f32 v[22:23], v[46:47], v[16:17] op_sel_hi:[0,1]
	v_pk_fma_f32 v[94:95], v[44:45], v[196:197], v[94:95] op_sel_hi:[0,1,1]
	v_exp_f32_e32 v21, v21
	v_pk_mul_f32 v[48:49], v[94:95], v[212:213]
	v_pk_mul_f32 v[88:89], v[88:89], v[24:25]
	v_exp_f32_e32 v22, v22
	v_pk_mul_f32 v[24:25], v[46:47], v[10:11] op_sel_hi:[0,1]
	v_pk_fma_f32 v[102:103], v[44:45], v[198:199], v[102:103] op_sel_hi:[0,1,1]
	v_exp_f32_e32 v23, v23
	v_pk_fma_f32 v[48:49], v[102:103], v[214:215], v[48:49]
	v_exp_f32_e32 v55, v55
	v_pk_mul_f32 v[96:97], v[96:97], v[26:27]
	v_exp_f32_e32 v24, v24
	v_pk_mul_f32 v[26:27], v[46:47], v[12:13] op_sel_hi:[0,1]
	v_pk_fma_f32 v[88:89], v[44:45], v[200:201], v[88:89] op_sel_hi:[0,1,1]
	v_exp_f32_e32 v25, v25
	v_pk_fma_f32 v[48:49], v[88:89], v[216:217], v[48:49]
	v_pk_mul_f32 v[90:91], v[90:91], v[28:29]
	v_exp_f32_e32 v26, v26
	v_pk_mul_f32 v[28:29], v[46:47], v[6:7] op_sel_hi:[0,1]
	v_pk_fma_f32 v[96:97], v[44:45], v[202:203], v[96:97] op_sel_hi:[0,1,1]
	v_exp_f32_e32 v27, v27
	v_pk_fma_f32 v[48:49], v[96:97], v[218:219], v[48:49]
	v_add_f32_e32 v55, 1.0, v55
	v_pk_mul_f32 v[92:93], v[92:93], v[30:31]
	v_exp_f32_e32 v28, v28
	v_pk_mul_f32 v[30:31], v[46:47], v[8:9] op_sel_hi:[0,1]
	v_pk_fma_f32 v[90:91], v[44:45], v[204:205], v[90:91] op_sel_hi:[0,1,1]
	v_exp_f32_e32 v29, v29
	v_pk_fma_f32 v[48:49], v[90:91], v[220:221], v[48:49]
	v_pk_mul_f32 v[98:99], v[98:99], v[32:33]
	v_exp_f32_e32 v30, v30
	v_pk_mul_f32 v[32:33], v[46:47], v[2:3] op_sel_hi:[0,1]
	v_pk_fma_f32 v[92:93], v[44:45], v[206:207], v[92:93] op_sel_hi:[0,1,1]
	v_exp_f32_e32 v31, v31
	v_pk_fma_f32 v[48:49], v[92:93], v[222:223], v[48:49]
	v_rcp_f32_e32 v55, v55
	v_pk_mul_f32 v[100:101], v[100:101], v[34:35]
	v_exp_f32_e32 v32, v32
	v_pk_mul_f32 v[34:35], v[46:47], v[4:5] op_sel_hi:[0,1]
	v_pk_fma_f32 v[98:99], v[44:45], v[208:209], v[98:99] op_sel_hi:[0,1,1]
	v_exp_f32_e32 v33, v33
	v_pk_fma_f32 v[48:49], v[98:99], v[224:225], v[48:49]
	v_exp_f32_e32 v34, v34
	v_pk_fma_f32 v[100:101], v[44:45], v[210:211], v[100:101] op_sel_hi:[0,1,1]
	v_exp_f32_e32 v35, v35
	v_pk_fma_f32 v[48:49], v[100:101], v[226:227], v[48:49]
	v_add_f32_e32 v54, v48, v49
	v_fma_mix_f32 v54, v87, v185, v54 op_sel:[0,1,0] op_sel_hi:[0,1,0]
	v_mul_f32_e32 v54, v54, v53
	v_fma_mix_f32 v44, v186, v186, 0 op_sel:[0,1,0] op_sel_hi:[1,1,0]
	v_fma_mixlo_f16 v56, v54, v55, 0
	ds_write_b16 v19, v56
	v_add_u32_e32 v19, 0x210, v19
	s_waitcnt lgkmcnt(1)
	ds_read_b128 v[196:199], v57 offset:448
	ds_read_b128 v[200:203], v57 offset:464
	ds_read_b128 v[204:207], v57 offset:480
	ds_read_b128 v[208:211], v57 offset:496
	ds_read_b128 v[212:215], v57 offset:4544
	ds_read_b128 v[216:219], v57 offset:4560
	ds_read_b128 v[220:223], v57 offset:4576
	ds_read_b128 v[224:227], v57 offset:4592
	v_cvt_f32_f16_e32 v46, v187
	v_cvt_f32_f16_e32 v53, v52
	ds_read_u16 v52, v19 offset:528
	v_pk_mul_f32 v[94:95], v[94:95], v[20:21]
	v_pk_mul_f32 v[20:21], v[46:47], v[14:15] op_sel_hi:[0,1]
	v_mul_f32_e32 v55, 0xbfb8aa3b, v53
	v_pk_mul_f32 v[102:103], v[102:103], v[22:23]
	v_exp_f32_e32 v20, v20
	v_pk_mul_f32 v[22:23], v[46:47], v[16:17] op_sel_hi:[0,1]
	v_pk_fma_f32 v[94:95], v[44:45], v[116:117], v[94:95] op_sel_hi:[0,1,1]
	v_exp_f32_e32 v21, v21
	v_pk_mul_f32 v[48:49], v[94:95], v[132:133]
	v_pk_mul_f32 v[88:89], v[88:89], v[24:25]
	v_exp_f32_e32 v22, v22
	v_pk_mul_f32 v[24:25], v[46:47], v[10:11] op_sel_hi:[0,1]
	v_pk_fma_f32 v[102:103], v[44:45], v[118:119], v[102:103] op_sel_hi:[0,1,1]
	v_exp_f32_e32 v23, v23
	v_pk_fma_f32 v[48:49], v[102:103], v[134:135], v[48:49]
	v_exp_f32_e32 v55, v55
	v_pk_mul_f32 v[96:97], v[96:97], v[26:27]
	v_exp_f32_e32 v24, v24
	v_pk_mul_f32 v[26:27], v[46:47], v[12:13] op_sel_hi:[0,1]
	v_pk_fma_f32 v[88:89], v[44:45], v[120:121], v[88:89] op_sel_hi:[0,1,1]
	v_exp_f32_e32 v25, v25
	v_pk_fma_f32 v[48:49], v[88:89], v[136:137], v[48:49]
	v_pk_mul_f32 v[90:91], v[90:91], v[28:29]
	v_exp_f32_e32 v26, v26
	v_pk_mul_f32 v[28:29], v[46:47], v[6:7] op_sel_hi:[0,1]
	v_pk_fma_f32 v[96:97], v[44:45], v[122:123], v[96:97] op_sel_hi:[0,1,1]
	v_exp_f32_e32 v27, v27
	v_pk_fma_f32 v[48:49], v[96:97], v[138:139], v[48:49]
	v_add_f32_e32 v55, 1.0, v55
	v_pk_mul_f32 v[92:93], v[92:93], v[30:31]
	v_exp_f32_e32 v28, v28
	v_pk_mul_f32 v[30:31], v[46:47], v[8:9] op_sel_hi:[0,1]
	v_pk_fma_f32 v[90:91], v[44:45], v[124:125], v[90:91] op_sel_hi:[0,1,1]
	v_exp_f32_e32 v29, v29
	v_pk_fma_f32 v[48:49], v[90:91], v[140:141], v[48:49]
	v_pk_mul_f32 v[98:99], v[98:99], v[32:33]
	v_exp_f32_e32 v30, v30
	v_pk_mul_f32 v[32:33], v[46:47], v[2:3] op_sel_hi:[0,1]
	v_pk_fma_f32 v[92:93], v[44:45], v[126:127], v[92:93] op_sel_hi:[0,1,1]
	v_exp_f32_e32 v31, v31
	v_pk_fma_f32 v[48:49], v[92:93], v[142:143], v[48:49]
	v_rcp_f32_e32 v55, v55
	v_pk_mul_f32 v[100:101], v[100:101], v[34:35]
	v_exp_f32_e32 v32, v32
	v_pk_mul_f32 v[34:35], v[46:47], v[4:5] op_sel_hi:[0,1]
	v_pk_fma_f32 v[98:99], v[44:45], v[128:129], v[98:99] op_sel_hi:[0,1,1]
	v_exp_f32_e32 v33, v33
	v_pk_fma_f32 v[48:49], v[98:99], v[144:145], v[48:49]
	v_exp_f32_e32 v34, v34
	v_pk_fma_f32 v[100:101], v[44:45], v[130:131], v[100:101] op_sel_hi:[0,1,1]
	v_exp_f32_e32 v35, v35
	v_pk_fma_f32 v[48:49], v[100:101], v[146:147], v[48:49]
	v_add_f32_e32 v54, v48, v49
	v_fma_mix_f32 v54, v87, v186, v54 op_sel:[0,1,0] op_sel_hi:[0,1,0]
	v_mul_f32_e32 v54, v54, v53
	v_fma_mix_f32 v44, v187, v187, 0 op_sel:[0,1,0] op_sel_hi:[1,1,0]
	v_fma_mixlo_f16 v56, v54, v55, 0
	ds_write_b16 v19, v56
	v_add_u32_e32 v19, 0x210, v19
	s_waitcnt lgkmcnt(1)
	ds_read_b128 v[116:119], v57 offset:512
	ds_read_b128 v[120:123], v57 offset:528
	ds_read_b128 v[124:127], v57 offset:544
	ds_read_b128 v[128:131], v57 offset:560
	ds_read_b128 v[132:135], v57 offset:4608
	ds_read_b128 v[136:139], v57 offset:4624
	ds_read_b128 v[140:143], v57 offset:4640
	ds_read_b128 v[144:147], v57 offset:4656
	s_waitcnt vmcnt(2)
	v_cvt_f32_f16_e32 v46, v188
	v_cvt_f32_f16_e32 v53, v52
	ds_read_u16 v52, v19 offset:528
	v_pk_mul_f32 v[94:95], v[94:95], v[20:21]
	v_pk_mul_f32 v[20:21], v[46:47], v[14:15] op_sel_hi:[0,1]
	v_mul_f32_e32 v55, 0xbfb8aa3b, v53
	v_pk_mul_f32 v[102:103], v[102:103], v[22:23]
	v_exp_f32_e32 v20, v20
	v_pk_mul_f32 v[22:23], v[46:47], v[16:17] op_sel_hi:[0,1]
	v_pk_fma_f32 v[94:95], v[44:45], v[196:197], v[94:95] op_sel_hi:[0,1,1]
	v_exp_f32_e32 v21, v21
	v_pk_mul_f32 v[48:49], v[94:95], v[212:213]
	v_pk_mul_f32 v[88:89], v[88:89], v[24:25]
	v_exp_f32_e32 v22, v22
	v_pk_mul_f32 v[24:25], v[46:47], v[10:11] op_sel_hi:[0,1]
	v_pk_fma_f32 v[102:103], v[44:45], v[198:199], v[102:103] op_sel_hi:[0,1,1]
	v_exp_f32_e32 v23, v23
	v_pk_fma_f32 v[48:49], v[102:103], v[214:215], v[48:49]
	v_exp_f32_e32 v55, v55
	v_pk_mul_f32 v[96:97], v[96:97], v[26:27]
	v_exp_f32_e32 v24, v24
	v_pk_mul_f32 v[26:27], v[46:47], v[12:13] op_sel_hi:[0,1]
	v_pk_fma_f32 v[88:89], v[44:45], v[200:201], v[88:89] op_sel_hi:[0,1,1]
	v_exp_f32_e32 v25, v25
	v_pk_fma_f32 v[48:49], v[88:89], v[216:217], v[48:49]
	v_pk_mul_f32 v[90:91], v[90:91], v[28:29]
	v_exp_f32_e32 v26, v26
	v_pk_mul_f32 v[28:29], v[46:47], v[6:7] op_sel_hi:[0,1]
	v_pk_fma_f32 v[96:97], v[44:45], v[202:203], v[96:97] op_sel_hi:[0,1,1]
	v_exp_f32_e32 v27, v27
	v_pk_fma_f32 v[48:49], v[96:97], v[218:219], v[48:49]
	v_add_f32_e32 v55, 1.0, v55
	v_pk_mul_f32 v[92:93], v[92:93], v[30:31]
	v_exp_f32_e32 v28, v28
	v_pk_mul_f32 v[30:31], v[46:47], v[8:9] op_sel_hi:[0,1]
	v_pk_fma_f32 v[90:91], v[44:45], v[204:205], v[90:91] op_sel_hi:[0,1,1]
	v_exp_f32_e32 v29, v29
	v_pk_fma_f32 v[48:49], v[90:91], v[220:221], v[48:49]
	v_pk_mul_f32 v[98:99], v[98:99], v[32:33]
	v_exp_f32_e32 v30, v30
	v_pk_mul_f32 v[32:33], v[46:47], v[2:3] op_sel_hi:[0,1]
	v_pk_fma_f32 v[92:93], v[44:45], v[206:207], v[92:93] op_sel_hi:[0,1,1]
	v_exp_f32_e32 v31, v31
	v_pk_fma_f32 v[48:49], v[92:93], v[222:223], v[48:49]
	v_rcp_f32_e32 v55, v55
	v_pk_mul_f32 v[100:101], v[100:101], v[34:35]
	v_exp_f32_e32 v32, v32
	v_pk_mul_f32 v[34:35], v[46:47], v[4:5] op_sel_hi:[0,1]
	v_pk_fma_f32 v[98:99], v[44:45], v[208:209], v[98:99] op_sel_hi:[0,1,1]
	v_exp_f32_e32 v33, v33
	v_pk_fma_f32 v[48:49], v[98:99], v[224:225], v[48:49]
	v_exp_f32_e32 v34, v34
	v_pk_fma_f32 v[100:101], v[44:45], v[210:211], v[100:101] op_sel_hi:[0,1,1]
	v_exp_f32_e32 v35, v35
	v_pk_fma_f32 v[48:49], v[100:101], v[226:227], v[48:49]
	v_add_f32_e32 v54, v48, v49
	v_fma_mix_f32 v54, v87, v187, v54 op_sel:[0,1,0] op_sel_hi:[0,1,0]
	v_mul_f32_e32 v54, v54, v53
	v_fma_mix_f32 v44, v188, v188, 0 op_sel:[0,1,0] op_sel_hi:[1,1,0]
	global_load_dwordx4 v[184:187], v[58:59], off nt
	v_fma_mixlo_f16 v56, v54, v55, 0
	ds_write_b16 v19, v56
	v_add_u32_e32 v19, 0x210, v19
	s_waitcnt lgkmcnt(1)
	ds_read_b128 v[196:199], v57 offset:576
	ds_read_b128 v[200:203], v57 offset:592
	ds_read_b128 v[204:207], v57 offset:608
	ds_read_b128 v[208:211], v57 offset:624
	ds_read_b128 v[212:215], v57 offset:4672
	ds_read_b128 v[216:219], v57 offset:4688
	ds_read_b128 v[220:223], v57 offset:4704
	ds_read_b128 v[224:227], v57 offset:4720
	v_cvt_f32_f16_e32 v46, v189
	v_cvt_f32_f16_e32 v53, v52
	ds_read_u16 v52, v19 offset:528
	v_pk_mul_f32 v[94:95], v[94:95], v[20:21]
	v_pk_mul_f32 v[20:21], v[46:47], v[14:15] op_sel_hi:[0,1]
	v_mul_f32_e32 v55, 0xbfb8aa3b, v53
	v_pk_mul_f32 v[102:103], v[102:103], v[22:23]
	v_exp_f32_e32 v20, v20
	v_pk_mul_f32 v[22:23], v[46:47], v[16:17] op_sel_hi:[0,1]
	v_pk_fma_f32 v[94:95], v[44:45], v[116:117], v[94:95] op_sel_hi:[0,1,1]
	v_exp_f32_e32 v21, v21
	v_pk_mul_f32 v[48:49], v[94:95], v[132:133]
	v_pk_mul_f32 v[88:89], v[88:89], v[24:25]
	v_exp_f32_e32 v22, v22
	v_pk_mul_f32 v[24:25], v[46:47], v[10:11] op_sel_hi:[0,1]
	v_pk_fma_f32 v[102:103], v[44:45], v[118:119], v[102:103] op_sel_hi:[0,1,1]
	v_exp_f32_e32 v23, v23
	v_pk_fma_f32 v[48:49], v[102:103], v[134:135], v[48:49]
	v_exp_f32_e32 v55, v55
	v_pk_mul_f32 v[96:97], v[96:97], v[26:27]
	v_exp_f32_e32 v24, v24
	v_pk_mul_f32 v[26:27], v[46:47], v[12:13] op_sel_hi:[0,1]
	v_pk_fma_f32 v[88:89], v[44:45], v[120:121], v[88:89] op_sel_hi:[0,1,1]
	v_exp_f32_e32 v25, v25
	v_pk_fma_f32 v[48:49], v[88:89], v[136:137], v[48:49]
	v_pk_mul_f32 v[90:91], v[90:91], v[28:29]
	v_exp_f32_e32 v26, v26
	v_pk_mul_f32 v[28:29], v[46:47], v[6:7] op_sel_hi:[0,1]
	v_pk_fma_f32 v[96:97], v[44:45], v[122:123], v[96:97] op_sel_hi:[0,1,1]
	v_exp_f32_e32 v27, v27
	v_pk_fma_f32 v[48:49], v[96:97], v[138:139], v[48:49]
	v_add_f32_e32 v55, 1.0, v55
	v_pk_mul_f32 v[92:93], v[92:93], v[30:31]
	v_exp_f32_e32 v28, v28
	v_pk_mul_f32 v[30:31], v[46:47], v[8:9] op_sel_hi:[0,1]
	v_pk_fma_f32 v[90:91], v[44:45], v[124:125], v[90:91] op_sel_hi:[0,1,1]
	v_exp_f32_e32 v29, v29
	v_pk_fma_f32 v[48:49], v[90:91], v[140:141], v[48:49]
	v_pk_mul_f32 v[98:99], v[98:99], v[32:33]
	v_exp_f32_e32 v30, v30
	v_pk_mul_f32 v[32:33], v[46:47], v[2:3] op_sel_hi:[0,1]
	v_pk_fma_f32 v[92:93], v[44:45], v[126:127], v[92:93] op_sel_hi:[0,1,1]
	v_exp_f32_e32 v31, v31
	v_pk_fma_f32 v[48:49], v[92:93], v[142:143], v[48:49]
	v_rcp_f32_e32 v55, v55
	v_pk_mul_f32 v[100:101], v[100:101], v[34:35]
	v_exp_f32_e32 v32, v32
	v_pk_mul_f32 v[34:35], v[46:47], v[4:5] op_sel_hi:[0,1]
	v_pk_fma_f32 v[98:99], v[44:45], v[128:129], v[98:99] op_sel_hi:[0,1,1]
	v_exp_f32_e32 v33, v33
	v_pk_fma_f32 v[48:49], v[98:99], v[144:145], v[48:49]
	v_exp_f32_e32 v34, v34
	v_pk_fma_f32 v[100:101], v[44:45], v[130:131], v[100:101] op_sel_hi:[0,1,1]
	v_exp_f32_e32 v35, v35
	v_pk_fma_f32 v[48:49], v[100:101], v[146:147], v[48:49]
	v_add_f32_e32 v54, v48, v49
	v_fma_mix_f32 v54, v87, v188, v54 op_sel:[0,1,0] op_sel_hi:[0,1,0]
	v_mul_f32_e32 v54, v54, v53
	v_fma_mix_f32 v44, v189, v189, 0 op_sel:[0,1,0] op_sel_hi:[1,1,0]
	v_fma_mixlo_f16 v56, v54, v55, 0
	ds_write_b16 v19, v56
	v_add_u32_e32 v19, 0x210, v19
	s_waitcnt lgkmcnt(1)
	ds_read_b128 v[116:119], v57 offset:640
	ds_read_b128 v[120:123], v57 offset:656
	ds_read_b128 v[124:127], v57 offset:672
	ds_read_b128 v[128:131], v57 offset:688
	ds_read_b128 v[132:135], v57 offset:4736
	ds_read_b128 v[136:139], v57 offset:4752
	ds_read_b128 v[140:143], v57 offset:4768
	ds_read_b128 v[144:147], v57 offset:4784
	v_cvt_f32_f16_e32 v46, v190
	v_cvt_f32_f16_e32 v53, v52
	ds_read_u16 v52, v19 offset:528
	v_pk_mul_f32 v[94:95], v[94:95], v[20:21]
	v_pk_mul_f32 v[20:21], v[46:47], v[14:15] op_sel_hi:[0,1]
	v_mul_f32_e32 v55, 0xbfb8aa3b, v53
	v_pk_mul_f32 v[102:103], v[102:103], v[22:23]
	v_exp_f32_e32 v20, v20
	v_pk_mul_f32 v[22:23], v[46:47], v[16:17] op_sel_hi:[0,1]
	v_pk_fma_f32 v[94:95], v[44:45], v[196:197], v[94:95] op_sel_hi:[0,1,1]
	v_exp_f32_e32 v21, v21
	v_pk_mul_f32 v[48:49], v[94:95], v[212:213]
	v_pk_mul_f32 v[88:89], v[88:89], v[24:25]
	v_exp_f32_e32 v22, v22
	v_pk_mul_f32 v[24:25], v[46:47], v[10:11] op_sel_hi:[0,1]
	v_pk_fma_f32 v[102:103], v[44:45], v[198:199], v[102:103] op_sel_hi:[0,1,1]
	v_exp_f32_e32 v23, v23
	v_pk_fma_f32 v[48:49], v[102:103], v[214:215], v[48:49]
	v_exp_f32_e32 v55, v55
	v_pk_mul_f32 v[96:97], v[96:97], v[26:27]
	v_exp_f32_e32 v24, v24
	v_pk_mul_f32 v[26:27], v[46:47], v[12:13] op_sel_hi:[0,1]
	v_pk_fma_f32 v[88:89], v[44:45], v[200:201], v[88:89] op_sel_hi:[0,1,1]
	v_exp_f32_e32 v25, v25
	v_pk_fma_f32 v[48:49], v[88:89], v[216:217], v[48:49]
	v_pk_mul_f32 v[90:91], v[90:91], v[28:29]
	v_exp_f32_e32 v26, v26
	v_pk_mul_f32 v[28:29], v[46:47], v[6:7] op_sel_hi:[0,1]
	v_pk_fma_f32 v[96:97], v[44:45], v[202:203], v[96:97] op_sel_hi:[0,1,1]
	v_exp_f32_e32 v27, v27
	v_pk_fma_f32 v[48:49], v[96:97], v[218:219], v[48:49]
	v_add_f32_e32 v55, 1.0, v55
	v_pk_mul_f32 v[92:93], v[92:93], v[30:31]
	v_exp_f32_e32 v28, v28
	v_pk_mul_f32 v[30:31], v[46:47], v[8:9] op_sel_hi:[0,1]
	v_pk_fma_f32 v[90:91], v[44:45], v[204:205], v[90:91] op_sel_hi:[0,1,1]
	v_exp_f32_e32 v29, v29
	v_pk_fma_f32 v[48:49], v[90:91], v[220:221], v[48:49]
	v_pk_mul_f32 v[98:99], v[98:99], v[32:33]
	v_exp_f32_e32 v30, v30
	v_pk_mul_f32 v[32:33], v[46:47], v[2:3] op_sel_hi:[0,1]
	v_pk_fma_f32 v[92:93], v[44:45], v[206:207], v[92:93] op_sel_hi:[0,1,1]
	v_exp_f32_e32 v31, v31
	v_pk_fma_f32 v[48:49], v[92:93], v[222:223], v[48:49]
	v_rcp_f32_e32 v55, v55
	v_pk_mul_f32 v[100:101], v[100:101], v[34:35]
	v_exp_f32_e32 v32, v32
	v_pk_mul_f32 v[34:35], v[46:47], v[4:5] op_sel_hi:[0,1]
	v_pk_fma_f32 v[98:99], v[44:45], v[208:209], v[98:99] op_sel_hi:[0,1,1]
	v_exp_f32_e32 v33, v33
	v_pk_fma_f32 v[48:49], v[98:99], v[224:225], v[48:49]
	v_exp_f32_e32 v34, v34
	v_pk_fma_f32 v[100:101], v[44:45], v[210:211], v[100:101] op_sel_hi:[0,1,1]
	v_exp_f32_e32 v35, v35
	v_pk_fma_f32 v[48:49], v[100:101], v[226:227], v[48:49]
	v_add_f32_e32 v54, v48, v49
	v_fma_mix_f32 v54, v87, v189, v54 op_sel:[0,1,0] op_sel_hi:[0,1,0]
	v_mul_f32_e32 v54, v54, v53
	v_fma_mix_f32 v44, v190, v190, 0 op_sel:[0,1,0] op_sel_hi:[1,1,0]
	v_fma_mixlo_f16 v56, v54, v55, 0
	ds_write_b16 v19, v56
	v_add_u32_e32 v19, 0x210, v19
	s_waitcnt lgkmcnt(1)
	ds_read_b128 v[196:199], v57 offset:704
	ds_read_b128 v[200:203], v57 offset:720
	ds_read_b128 v[204:207], v57 offset:736
	ds_read_b128 v[208:211], v57 offset:752
	ds_read_b128 v[212:215], v57 offset:4800
	ds_read_b128 v[216:219], v57 offset:4816
	ds_read_b128 v[220:223], v57 offset:4832
	ds_read_b128 v[224:227], v57 offset:4848
	v_cvt_f32_f16_e32 v46, v191
	v_cvt_f32_f16_e32 v53, v52
	ds_read_u16 v52, v19 offset:528
	v_pk_mul_f32 v[94:95], v[94:95], v[20:21]
	v_pk_mul_f32 v[20:21], v[46:47], v[14:15] op_sel_hi:[0,1]
	v_mul_f32_e32 v55, 0xbfb8aa3b, v53
	v_pk_mul_f32 v[102:103], v[102:103], v[22:23]
	v_exp_f32_e32 v20, v20
	v_pk_mul_f32 v[22:23], v[46:47], v[16:17] op_sel_hi:[0,1]
	v_pk_fma_f32 v[94:95], v[44:45], v[116:117], v[94:95] op_sel_hi:[0,1,1]
	v_exp_f32_e32 v21, v21
	v_pk_mul_f32 v[48:49], v[94:95], v[132:133]
	v_pk_mul_f32 v[88:89], v[88:89], v[24:25]
	v_exp_f32_e32 v22, v22
	v_pk_mul_f32 v[24:25], v[46:47], v[10:11] op_sel_hi:[0,1]
	v_pk_fma_f32 v[102:103], v[44:45], v[118:119], v[102:103] op_sel_hi:[0,1,1]
	v_exp_f32_e32 v23, v23
	v_pk_fma_f32 v[48:49], v[102:103], v[134:135], v[48:49]
	v_exp_f32_e32 v55, v55
	v_pk_mul_f32 v[96:97], v[96:97], v[26:27]
	v_exp_f32_e32 v24, v24
	v_pk_mul_f32 v[26:27], v[46:47], v[12:13] op_sel_hi:[0,1]
	v_pk_fma_f32 v[88:89], v[44:45], v[120:121], v[88:89] op_sel_hi:[0,1,1]
	v_exp_f32_e32 v25, v25
	v_pk_fma_f32 v[48:49], v[88:89], v[136:137], v[48:49]
	v_pk_mul_f32 v[90:91], v[90:91], v[28:29]
	v_exp_f32_e32 v26, v26
	v_pk_mul_f32 v[28:29], v[46:47], v[6:7] op_sel_hi:[0,1]
	v_pk_fma_f32 v[96:97], v[44:45], v[122:123], v[96:97] op_sel_hi:[0,1,1]
	v_exp_f32_e32 v27, v27
	v_pk_fma_f32 v[48:49], v[96:97], v[138:139], v[48:49]
	v_add_f32_e32 v55, 1.0, v55
	v_pk_mul_f32 v[92:93], v[92:93], v[30:31]
	v_exp_f32_e32 v28, v28
	v_pk_mul_f32 v[30:31], v[46:47], v[8:9] op_sel_hi:[0,1]
	v_pk_fma_f32 v[90:91], v[44:45], v[124:125], v[90:91] op_sel_hi:[0,1,1]
	v_exp_f32_e32 v29, v29
	v_pk_fma_f32 v[48:49], v[90:91], v[140:141], v[48:49]
	v_pk_mul_f32 v[98:99], v[98:99], v[32:33]
	v_exp_f32_e32 v30, v30
	v_pk_mul_f32 v[32:33], v[46:47], v[2:3] op_sel_hi:[0,1]
	v_pk_fma_f32 v[92:93], v[44:45], v[126:127], v[92:93] op_sel_hi:[0,1,1]
	v_exp_f32_e32 v31, v31
	v_pk_fma_f32 v[48:49], v[92:93], v[142:143], v[48:49]
	v_rcp_f32_e32 v55, v55
	v_pk_mul_f32 v[100:101], v[100:101], v[34:35]
	v_exp_f32_e32 v32, v32
	v_pk_mul_f32 v[34:35], v[46:47], v[4:5] op_sel_hi:[0,1]
	v_pk_fma_f32 v[98:99], v[44:45], v[128:129], v[98:99] op_sel_hi:[0,1,1]
	v_exp_f32_e32 v33, v33
	v_pk_fma_f32 v[48:49], v[98:99], v[144:145], v[48:49]
	v_exp_f32_e32 v34, v34
	v_pk_fma_f32 v[100:101], v[44:45], v[130:131], v[100:101] op_sel_hi:[0,1,1]
	v_exp_f32_e32 v35, v35
	v_pk_fma_f32 v[48:49], v[100:101], v[146:147], v[48:49]
	v_add_f32_e32 v54, v48, v49
	v_fma_mix_f32 v54, v87, v190, v54 op_sel:[0,1,0] op_sel_hi:[0,1,0]
	v_mul_f32_e32 v54, v54, v53
	v_fma_mix_f32 v44, v191, v191, 0 op_sel:[0,1,0] op_sel_hi:[1,1,0]
	v_fma_mixlo_f16 v56, v54, v55, 0
	ds_write_b16 v19, v56
	v_add_u32_e32 v19, 0x210, v19
	s_waitcnt lgkmcnt(1)
	ds_read_b128 v[116:119], v57 offset:768
	ds_read_b128 v[120:123], v57 offset:784
	ds_read_b128 v[124:127], v57 offset:800
	ds_read_b128 v[128:131], v57 offset:816
	ds_read_b128 v[132:135], v57 offset:4864
	ds_read_b128 v[136:139], v57 offset:4880
	ds_read_b128 v[140:143], v57 offset:4896
	ds_read_b128 v[144:147], v57 offset:4912
	s_waitcnt vmcnt(2)
	v_cvt_f32_f16_e32 v46, v192
	v_cvt_f32_f16_e32 v53, v52
	ds_read_u16 v52, v19 offset:528
	v_pk_mul_f32 v[94:95], v[94:95], v[20:21]
	v_pk_mul_f32 v[20:21], v[46:47], v[14:15] op_sel_hi:[0,1]
	v_mul_f32_e32 v55, 0xbfb8aa3b, v53
	v_pk_mul_f32 v[102:103], v[102:103], v[22:23]
	v_exp_f32_e32 v20, v20
	v_pk_mul_f32 v[22:23], v[46:47], v[16:17] op_sel_hi:[0,1]
	v_pk_fma_f32 v[94:95], v[44:45], v[196:197], v[94:95] op_sel_hi:[0,1,1]
	v_exp_f32_e32 v21, v21
	v_pk_mul_f32 v[48:49], v[94:95], v[212:213]
	v_pk_mul_f32 v[88:89], v[88:89], v[24:25]
	v_exp_f32_e32 v22, v22
	v_pk_mul_f32 v[24:25], v[46:47], v[10:11] op_sel_hi:[0,1]
	v_pk_fma_f32 v[102:103], v[44:45], v[198:199], v[102:103] op_sel_hi:[0,1,1]
	v_exp_f32_e32 v23, v23
	v_pk_fma_f32 v[48:49], v[102:103], v[214:215], v[48:49]
	v_exp_f32_e32 v55, v55
	v_pk_mul_f32 v[96:97], v[96:97], v[26:27]
	v_exp_f32_e32 v24, v24
	v_pk_mul_f32 v[26:27], v[46:47], v[12:13] op_sel_hi:[0,1]
	v_pk_fma_f32 v[88:89], v[44:45], v[200:201], v[88:89] op_sel_hi:[0,1,1]
	v_exp_f32_e32 v25, v25
	v_pk_fma_f32 v[48:49], v[88:89], v[216:217], v[48:49]
	v_pk_mul_f32 v[90:91], v[90:91], v[28:29]
	v_exp_f32_e32 v26, v26
	v_pk_mul_f32 v[28:29], v[46:47], v[6:7] op_sel_hi:[0,1]
	v_pk_fma_f32 v[96:97], v[44:45], v[202:203], v[96:97] op_sel_hi:[0,1,1]
	v_exp_f32_e32 v27, v27
	v_pk_fma_f32 v[48:49], v[96:97], v[218:219], v[48:49]
	v_add_f32_e32 v55, 1.0, v55
	v_pk_mul_f32 v[92:93], v[92:93], v[30:31]
	v_exp_f32_e32 v28, v28
	v_pk_mul_f32 v[30:31], v[46:47], v[8:9] op_sel_hi:[0,1]
	v_pk_fma_f32 v[90:91], v[44:45], v[204:205], v[90:91] op_sel_hi:[0,1,1]
	v_exp_f32_e32 v29, v29
	v_pk_fma_f32 v[48:49], v[90:91], v[220:221], v[48:49]
	v_pk_mul_f32 v[98:99], v[98:99], v[32:33]
	v_exp_f32_e32 v30, v30
	v_pk_mul_f32 v[32:33], v[46:47], v[2:3] op_sel_hi:[0,1]
	v_pk_fma_f32 v[92:93], v[44:45], v[206:207], v[92:93] op_sel_hi:[0,1,1]
	v_exp_f32_e32 v31, v31
	v_pk_fma_f32 v[48:49], v[92:93], v[222:223], v[48:49]
	v_rcp_f32_e32 v55, v55
	v_pk_mul_f32 v[100:101], v[100:101], v[34:35]
	v_exp_f32_e32 v32, v32
	v_pk_mul_f32 v[34:35], v[46:47], v[4:5] op_sel_hi:[0,1]
	v_pk_fma_f32 v[98:99], v[44:45], v[208:209], v[98:99] op_sel_hi:[0,1,1]
	v_exp_f32_e32 v33, v33
	v_pk_fma_f32 v[48:49], v[98:99], v[224:225], v[48:49]
	v_exp_f32_e32 v34, v34
	v_pk_fma_f32 v[100:101], v[44:45], v[210:211], v[100:101] op_sel_hi:[0,1,1]
	v_exp_f32_e32 v35, v35
	v_pk_fma_f32 v[48:49], v[100:101], v[226:227], v[48:49]
	v_add_f32_e32 v54, v48, v49
	v_fma_mix_f32 v54, v87, v191, v54 op_sel:[0,1,0] op_sel_hi:[0,1,0]
	v_mul_f32_e32 v54, v54, v53
	v_fma_mix_f32 v44, v192, v192, 0 op_sel:[0,1,0] op_sel_hi:[1,1,0]
	global_load_dwordx4 v[188:191], v[50:51], off offset:-4096 nt
	v_fma_mixlo_f16 v56, v54, v55, 0
	ds_write_b16 v19, v56
	v_add_u32_e32 v19, 0x210, v19
	s_waitcnt lgkmcnt(1)
	ds_read_b128 v[196:199], v57 offset:832
	ds_read_b128 v[200:203], v57 offset:848
	ds_read_b128 v[204:207], v57 offset:864
	ds_read_b128 v[208:211], v57 offset:880
	ds_read_b128 v[212:215], v57 offset:4928
	ds_read_b128 v[216:219], v57 offset:4944
	ds_read_b128 v[220:223], v57 offset:4960
	ds_read_b128 v[224:227], v57 offset:4976
	v_cvt_f32_f16_e32 v46, v193
	v_cvt_f32_f16_e32 v53, v52
	ds_read_u16 v52, v19 offset:528
	v_pk_mul_f32 v[94:95], v[94:95], v[20:21]
	v_pk_mul_f32 v[20:21], v[46:47], v[14:15] op_sel_hi:[0,1]
	v_mul_f32_e32 v55, 0xbfb8aa3b, v53
	v_pk_mul_f32 v[102:103], v[102:103], v[22:23]
	v_exp_f32_e32 v20, v20
	v_pk_mul_f32 v[22:23], v[46:47], v[16:17] op_sel_hi:[0,1]
	v_pk_fma_f32 v[94:95], v[44:45], v[116:117], v[94:95] op_sel_hi:[0,1,1]
	v_exp_f32_e32 v21, v21
	v_pk_mul_f32 v[48:49], v[94:95], v[132:133]
	v_pk_mul_f32 v[88:89], v[88:89], v[24:25]
	v_exp_f32_e32 v22, v22
	v_pk_mul_f32 v[24:25], v[46:47], v[10:11] op_sel_hi:[0,1]
	v_pk_fma_f32 v[102:103], v[44:45], v[118:119], v[102:103] op_sel_hi:[0,1,1]
	v_exp_f32_e32 v23, v23
	v_pk_fma_f32 v[48:49], v[102:103], v[134:135], v[48:49]
	v_exp_f32_e32 v55, v55
	v_pk_mul_f32 v[96:97], v[96:97], v[26:27]
	v_exp_f32_e32 v24, v24
	v_pk_mul_f32 v[26:27], v[46:47], v[12:13] op_sel_hi:[0,1]
	v_pk_fma_f32 v[88:89], v[44:45], v[120:121], v[88:89] op_sel_hi:[0,1,1]
	v_exp_f32_e32 v25, v25
	v_pk_fma_f32 v[48:49], v[88:89], v[136:137], v[48:49]
	v_pk_mul_f32 v[90:91], v[90:91], v[28:29]
	v_exp_f32_e32 v26, v26
	v_pk_mul_f32 v[28:29], v[46:47], v[6:7] op_sel_hi:[0,1]
	v_pk_fma_f32 v[96:97], v[44:45], v[122:123], v[96:97] op_sel_hi:[0,1,1]
	v_exp_f32_e32 v27, v27
	v_pk_fma_f32 v[48:49], v[96:97], v[138:139], v[48:49]
	v_add_f32_e32 v55, 1.0, v55
	v_pk_mul_f32 v[92:93], v[92:93], v[30:31]
	v_exp_f32_e32 v28, v28
	v_pk_mul_f32 v[30:31], v[46:47], v[8:9] op_sel_hi:[0,1]
	v_pk_fma_f32 v[90:91], v[44:45], v[124:125], v[90:91] op_sel_hi:[0,1,1]
	v_exp_f32_e32 v29, v29
	v_pk_fma_f32 v[48:49], v[90:91], v[140:141], v[48:49]
	v_pk_mul_f32 v[98:99], v[98:99], v[32:33]
	v_exp_f32_e32 v30, v30
	v_pk_mul_f32 v[32:33], v[46:47], v[2:3] op_sel_hi:[0,1]
	v_pk_fma_f32 v[92:93], v[44:45], v[126:127], v[92:93] op_sel_hi:[0,1,1]
	v_exp_f32_e32 v31, v31
	v_pk_fma_f32 v[48:49], v[92:93], v[142:143], v[48:49]
	v_rcp_f32_e32 v55, v55
	v_pk_mul_f32 v[100:101], v[100:101], v[34:35]
	v_exp_f32_e32 v32, v32
	v_pk_mul_f32 v[34:35], v[46:47], v[4:5] op_sel_hi:[0,1]
	v_pk_fma_f32 v[98:99], v[44:45], v[128:129], v[98:99] op_sel_hi:[0,1,1]
	v_exp_f32_e32 v33, v33
	v_pk_fma_f32 v[48:49], v[98:99], v[144:145], v[48:49]
	v_exp_f32_e32 v34, v34
	v_pk_fma_f32 v[100:101], v[44:45], v[130:131], v[100:101] op_sel_hi:[0,1,1]
	v_exp_f32_e32 v35, v35
	v_pk_fma_f32 v[48:49], v[100:101], v[146:147], v[48:49]
	v_add_f32_e32 v54, v48, v49
	v_fma_mix_f32 v54, v87, v192, v54 op_sel:[0,1,0] op_sel_hi:[0,1,0]
	v_mul_f32_e32 v54, v54, v53
	v_fma_mix_f32 v44, v193, v193, 0 op_sel:[0,1,0] op_sel_hi:[1,1,0]
	v_fma_mixlo_f16 v56, v54, v55, 0
	ds_write_b16 v19, v56
	v_add_u32_e32 v19, 0x210, v19
	s_waitcnt lgkmcnt(1)
	ds_read_b128 v[116:119], v57 offset:896
	ds_read_b128 v[120:123], v57 offset:912
	ds_read_b128 v[124:127], v57 offset:928
	ds_read_b128 v[128:131], v57 offset:944
	ds_read_b128 v[132:135], v57 offset:4992
	ds_read_b128 v[136:139], v57 offset:5008
	ds_read_b128 v[140:143], v57 offset:5024
	ds_read_b128 v[144:147], v57 offset:5040
	v_cvt_f32_f16_e32 v46, v194
	v_cvt_f32_f16_e32 v53, v52
	ds_read_u16 v52, v19 offset:528
	v_pk_mul_f32 v[94:95], v[94:95], v[20:21]
	v_pk_mul_f32 v[20:21], v[46:47], v[14:15] op_sel_hi:[0,1]
	v_mul_f32_e32 v55, 0xbfb8aa3b, v53
	v_pk_mul_f32 v[102:103], v[102:103], v[22:23]
	v_exp_f32_e32 v20, v20
	v_pk_mul_f32 v[22:23], v[46:47], v[16:17] op_sel_hi:[0,1]
	v_pk_fma_f32 v[94:95], v[44:45], v[196:197], v[94:95] op_sel_hi:[0,1,1]
	v_exp_f32_e32 v21, v21
	v_pk_mul_f32 v[48:49], v[94:95], v[212:213]
	v_pk_mul_f32 v[88:89], v[88:89], v[24:25]
	v_exp_f32_e32 v22, v22
	v_pk_mul_f32 v[24:25], v[46:47], v[10:11] op_sel_hi:[0,1]
	v_pk_fma_f32 v[102:103], v[44:45], v[198:199], v[102:103] op_sel_hi:[0,1,1]
	v_exp_f32_e32 v23, v23
	v_pk_fma_f32 v[48:49], v[102:103], v[214:215], v[48:49]
	v_exp_f32_e32 v55, v55
	v_pk_mul_f32 v[96:97], v[96:97], v[26:27]
	v_exp_f32_e32 v24, v24
	v_pk_mul_f32 v[26:27], v[46:47], v[12:13] op_sel_hi:[0,1]
	v_pk_fma_f32 v[88:89], v[44:45], v[200:201], v[88:89] op_sel_hi:[0,1,1]
	v_exp_f32_e32 v25, v25
	v_pk_fma_f32 v[48:49], v[88:89], v[216:217], v[48:49]
	v_pk_mul_f32 v[90:91], v[90:91], v[28:29]
	v_exp_f32_e32 v26, v26
	v_pk_mul_f32 v[28:29], v[46:47], v[6:7] op_sel_hi:[0,1]
	v_pk_fma_f32 v[96:97], v[44:45], v[202:203], v[96:97] op_sel_hi:[0,1,1]
	v_exp_f32_e32 v27, v27
	v_pk_fma_f32 v[48:49], v[96:97], v[218:219], v[48:49]
	v_add_f32_e32 v55, 1.0, v55
	v_pk_mul_f32 v[92:93], v[92:93], v[30:31]
	v_exp_f32_e32 v28, v28
	v_pk_mul_f32 v[30:31], v[46:47], v[8:9] op_sel_hi:[0,1]
	v_pk_fma_f32 v[90:91], v[44:45], v[204:205], v[90:91] op_sel_hi:[0,1,1]
	v_exp_f32_e32 v29, v29
	v_pk_fma_f32 v[48:49], v[90:91], v[220:221], v[48:49]
	v_pk_mul_f32 v[98:99], v[98:99], v[32:33]
	v_exp_f32_e32 v30, v30
	v_pk_mul_f32 v[32:33], v[46:47], v[2:3] op_sel_hi:[0,1]
	v_pk_fma_f32 v[92:93], v[44:45], v[206:207], v[92:93] op_sel_hi:[0,1,1]
	v_exp_f32_e32 v31, v31
	v_pk_fma_f32 v[48:49], v[92:93], v[222:223], v[48:49]
	v_rcp_f32_e32 v55, v55
	v_pk_mul_f32 v[100:101], v[100:101], v[34:35]
	v_exp_f32_e32 v32, v32
	v_pk_mul_f32 v[34:35], v[46:47], v[4:5] op_sel_hi:[0,1]
	v_pk_fma_f32 v[98:99], v[44:45], v[208:209], v[98:99] op_sel_hi:[0,1,1]
	v_exp_f32_e32 v33, v33
	v_pk_fma_f32 v[48:49], v[98:99], v[224:225], v[48:49]
	v_exp_f32_e32 v34, v34
	v_pk_fma_f32 v[100:101], v[44:45], v[210:211], v[100:101] op_sel_hi:[0,1,1]
	v_exp_f32_e32 v35, v35
	v_pk_fma_f32 v[48:49], v[100:101], v[226:227], v[48:49]
	v_add_f32_e32 v54, v48, v49
	v_fma_mix_f32 v54, v87, v193, v54 op_sel:[0,1,0] op_sel_hi:[0,1,0]
	v_mul_f32_e32 v54, v54, v53
	v_fma_mix_f32 v44, v194, v194, 0 op_sel:[0,1,0] op_sel_hi:[1,1,0]
	v_fma_mixlo_f16 v56, v54, v55, 0
	ds_write_b16 v19, v56
	v_add_u32_e32 v19, 0x210, v19
	s_waitcnt lgkmcnt(1)
	ds_read_b128 v[196:199], v57 offset:960
	ds_read_b128 v[200:203], v57 offset:976
	ds_read_b128 v[204:207], v57 offset:992
	ds_read_b128 v[208:211], v57 offset:1008
	ds_read_b128 v[212:215], v57 offset:5056
	ds_read_b128 v[216:219], v57 offset:5072
	ds_read_b128 v[220:223], v57 offset:5088
	ds_read_b128 v[224:227], v57 offset:5104
	v_cvt_f32_f16_e32 v46, v195
	v_cvt_f32_f16_e32 v53, v52
	ds_read_u16 v52, v19 offset:528
	v_pk_mul_f32 v[94:95], v[94:95], v[20:21]
	v_pk_mul_f32 v[20:21], v[46:47], v[14:15] op_sel_hi:[0,1]
	v_mul_f32_e32 v55, 0xbfb8aa3b, v53
	v_pk_mul_f32 v[102:103], v[102:103], v[22:23]
	v_exp_f32_e32 v20, v20
	v_pk_mul_f32 v[22:23], v[46:47], v[16:17] op_sel_hi:[0,1]
	v_pk_fma_f32 v[94:95], v[44:45], v[116:117], v[94:95] op_sel_hi:[0,1,1]
	v_exp_f32_e32 v21, v21
	v_pk_mul_f32 v[48:49], v[94:95], v[132:133]
	v_pk_mul_f32 v[88:89], v[88:89], v[24:25]
	v_exp_f32_e32 v22, v22
	v_pk_mul_f32 v[24:25], v[46:47], v[10:11] op_sel_hi:[0,1]
	v_pk_fma_f32 v[102:103], v[44:45], v[118:119], v[102:103] op_sel_hi:[0,1,1]
	v_exp_f32_e32 v23, v23
	v_pk_fma_f32 v[48:49], v[102:103], v[134:135], v[48:49]
	v_exp_f32_e32 v55, v55
	v_pk_mul_f32 v[96:97], v[96:97], v[26:27]
	v_exp_f32_e32 v24, v24
	v_pk_mul_f32 v[26:27], v[46:47], v[12:13] op_sel_hi:[0,1]
	v_pk_fma_f32 v[88:89], v[44:45], v[120:121], v[88:89] op_sel_hi:[0,1,1]
	v_exp_f32_e32 v25, v25
	v_pk_fma_f32 v[48:49], v[88:89], v[136:137], v[48:49]
	v_pk_mul_f32 v[90:91], v[90:91], v[28:29]
	v_exp_f32_e32 v26, v26
	v_pk_mul_f32 v[28:29], v[46:47], v[6:7] op_sel_hi:[0,1]
	v_pk_fma_f32 v[96:97], v[44:45], v[122:123], v[96:97] op_sel_hi:[0,1,1]
	v_exp_f32_e32 v27, v27
	v_pk_fma_f32 v[48:49], v[96:97], v[138:139], v[48:49]
	v_add_f32_e32 v55, 1.0, v55
	v_pk_mul_f32 v[92:93], v[92:93], v[30:31]
	v_exp_f32_e32 v28, v28
	v_pk_mul_f32 v[30:31], v[46:47], v[8:9] op_sel_hi:[0,1]
	v_pk_fma_f32 v[90:91], v[44:45], v[124:125], v[90:91] op_sel_hi:[0,1,1]
	v_exp_f32_e32 v29, v29
	v_pk_fma_f32 v[48:49], v[90:91], v[140:141], v[48:49]
	v_pk_mul_f32 v[98:99], v[98:99], v[32:33]
	v_exp_f32_e32 v30, v30
	v_pk_mul_f32 v[32:33], v[46:47], v[2:3] op_sel_hi:[0,1]
	v_pk_fma_f32 v[92:93], v[44:45], v[126:127], v[92:93] op_sel_hi:[0,1,1]
	v_exp_f32_e32 v31, v31
	v_pk_fma_f32 v[48:49], v[92:93], v[142:143], v[48:49]
	v_rcp_f32_e32 v55, v55
	v_pk_mul_f32 v[100:101], v[100:101], v[34:35]
	v_exp_f32_e32 v32, v32
	v_pk_mul_f32 v[34:35], v[46:47], v[4:5] op_sel_hi:[0,1]
	v_pk_fma_f32 v[98:99], v[44:45], v[128:129], v[98:99] op_sel_hi:[0,1,1]
	v_exp_f32_e32 v33, v33
	v_pk_fma_f32 v[48:49], v[98:99], v[144:145], v[48:49]
	v_exp_f32_e32 v34, v34
	v_pk_fma_f32 v[100:101], v[44:45], v[130:131], v[100:101] op_sel_hi:[0,1,1]
	v_exp_f32_e32 v35, v35
	v_pk_fma_f32 v[48:49], v[100:101], v[146:147], v[48:49]
	v_add_f32_e32 v54, v48, v49
	v_fma_mix_f32 v54, v87, v194, v54 op_sel:[0,1,0] op_sel_hi:[0,1,0]
	v_mul_f32_e32 v54, v54, v53
	v_fma_mix_f32 v44, v195, v195, 0 op_sel:[0,1,0] op_sel_hi:[1,1,0]
	v_fma_mixlo_f16 v56, v54, v55, 0
	ds_write_b16 v19, v56
	v_add_u32_e32 v19, 0x210, v19
	s_waitcnt lgkmcnt(1)
	ds_read_b128 v[116:119], v57 offset:1024
	ds_read_b128 v[120:123], v57 offset:1040
	ds_read_b128 v[124:127], v57 offset:1056
	ds_read_b128 v[128:131], v57 offset:1072
	ds_read_b128 v[132:135], v57 offset:5120
	ds_read_b128 v[136:139], v57 offset:5136
	ds_read_b128 v[140:143], v57 offset:5152
	ds_read_b128 v[144:147], v57 offset:5168
	s_waitcnt vmcnt(2)
	v_cvt_f32_f16_e32 v46, v180
	v_cvt_f32_f16_e32 v53, v52
	ds_read_u16 v52, v19 offset:528
	v_pk_mul_f32 v[94:95], v[94:95], v[20:21]
	v_pk_mul_f32 v[20:21], v[46:47], v[14:15] op_sel_hi:[0,1]
	v_mul_f32_e32 v55, 0xbfb8aa3b, v53
	v_pk_mul_f32 v[102:103], v[102:103], v[22:23]
	v_exp_f32_e32 v20, v20
	v_pk_mul_f32 v[22:23], v[46:47], v[16:17] op_sel_hi:[0,1]
	v_pk_fma_f32 v[94:95], v[44:45], v[196:197], v[94:95] op_sel_hi:[0,1,1]
	v_exp_f32_e32 v21, v21
	v_pk_mul_f32 v[48:49], v[94:95], v[212:213]
	v_pk_mul_f32 v[88:89], v[88:89], v[24:25]
	v_exp_f32_e32 v22, v22
	v_pk_mul_f32 v[24:25], v[46:47], v[10:11] op_sel_hi:[0,1]
	v_pk_fma_f32 v[102:103], v[44:45], v[198:199], v[102:103] op_sel_hi:[0,1,1]
	v_exp_f32_e32 v23, v23
	v_pk_fma_f32 v[48:49], v[102:103], v[214:215], v[48:49]
	v_exp_f32_e32 v55, v55
	v_pk_mul_f32 v[96:97], v[96:97], v[26:27]
	v_exp_f32_e32 v24, v24
	v_pk_mul_f32 v[26:27], v[46:47], v[12:13] op_sel_hi:[0,1]
	v_pk_fma_f32 v[88:89], v[44:45], v[200:201], v[88:89] op_sel_hi:[0,1,1]
	v_exp_f32_e32 v25, v25
	v_pk_fma_f32 v[48:49], v[88:89], v[216:217], v[48:49]
	v_pk_mul_f32 v[90:91], v[90:91], v[28:29]
	v_exp_f32_e32 v26, v26
	v_pk_mul_f32 v[28:29], v[46:47], v[6:7] op_sel_hi:[0,1]
	v_pk_fma_f32 v[96:97], v[44:45], v[202:203], v[96:97] op_sel_hi:[0,1,1]
	v_exp_f32_e32 v27, v27
	v_pk_fma_f32 v[48:49], v[96:97], v[218:219], v[48:49]
	v_add_f32_e32 v55, 1.0, v55
	v_pk_mul_f32 v[92:93], v[92:93], v[30:31]
	v_exp_f32_e32 v28, v28
	v_pk_mul_f32 v[30:31], v[46:47], v[8:9] op_sel_hi:[0,1]
	v_pk_fma_f32 v[90:91], v[44:45], v[204:205], v[90:91] op_sel_hi:[0,1,1]
	v_exp_f32_e32 v29, v29
	v_pk_fma_f32 v[48:49], v[90:91], v[220:221], v[48:49]
	v_pk_mul_f32 v[98:99], v[98:99], v[32:33]
	v_exp_f32_e32 v30, v30
	v_pk_mul_f32 v[32:33], v[46:47], v[2:3] op_sel_hi:[0,1]
	v_pk_fma_f32 v[92:93], v[44:45], v[206:207], v[92:93] op_sel_hi:[0,1,1]
	v_exp_f32_e32 v31, v31
	v_pk_fma_f32 v[48:49], v[92:93], v[222:223], v[48:49]
	v_rcp_f32_e32 v55, v55
	v_pk_mul_f32 v[100:101], v[100:101], v[34:35]
	v_exp_f32_e32 v32, v32
	v_pk_mul_f32 v[34:35], v[46:47], v[4:5] op_sel_hi:[0,1]
	v_pk_fma_f32 v[98:99], v[44:45], v[208:209], v[98:99] op_sel_hi:[0,1,1]
	v_exp_f32_e32 v33, v33
	v_pk_fma_f32 v[48:49], v[98:99], v[224:225], v[48:49]
	v_exp_f32_e32 v34, v34
	v_pk_fma_f32 v[100:101], v[44:45], v[210:211], v[100:101] op_sel_hi:[0,1,1]
	v_exp_f32_e32 v35, v35
	v_pk_fma_f32 v[48:49], v[100:101], v[226:227], v[48:49]
	v_add_f32_e32 v54, v48, v49
	v_fma_mix_f32 v54, v87, v195, v54 op_sel:[0,1,0] op_sel_hi:[0,1,0]
	v_mul_f32_e32 v54, v54, v53
	v_fma_mix_f32 v44, v180, v180, 0 op_sel:[0,1,0] op_sel_hi:[1,1,0]
	global_load_dwordx4 v[192:195], v[50:51], off nt
	v_fma_mixlo_f16 v56, v54, v55, 0
	ds_write_b16 v19, v56
	v_add_u32_e32 v19, 0x210, v19
	v_add_u32_e32 v57, 0x400, v57
	v_lshl_add_u64 v[58:59], v[58:59], 0, s[10:11]
	v_lshl_add_u64 v[50:51], v[50:51], 0, s[10:11]
	s_add_i32 s12, s12, 1
	s_cmp_eq_u32 s12, 4
	s_cbranch_scc0 .Lsc3_loop
	global_load_dwordx4 v[18:21], v86, s[4:5]
	global_load_dwordx4 v[34:37], v86, s[4:5] offset:1024
	global_load_dwordx4 v[38:41], v86, s[4:5] offset:2048
	global_load_dwordx4 v[42:45], v86, s[4:5] offset:3072
	v_mov_b32_e32 v87, 0
	v_and_b32_e32 v112, 31, v0
	v_lshl_add_u64 v[2:3], s[4:5], 0, v[86:87]
	v_and_b32_e32 v5, 8, v114
	v_mul_u32_u24_e32 v6, 0x210, v112
	v_add_co_u32_e32 v4, vcc, 0x1000, v2
	v_lshl_add_u32 v113, v5, 1, v6
	s_nop 0
	v_addc_co_u32_e32 v5, vcc, 0, v3, vcc
	global_load_dwordx4 v[46:49], v[4:5], off
	global_load_dwordx4 v[50:53], v[4:5], off offset:1024
	global_load_dwordx4 v[54:57], v[4:5], off offset:2048
	global_load_dwordx4 v[58:61], v[4:5], off offset:3072
	v_add_co_u32_e32 v6, vcc, 0x2000, v2
	s_movk_i32 s4, 0x110
	s_nop 0
	v_addc_co_u32_e32 v7, vcc, 0, v3, vcc
	global_load_dwordx4 v[62:65], v[6:7], off
	global_load_dwordx4 v[66:69], v[6:7], off offset:1024
	global_load_dwordx4 v[70:73], v[6:7], off offset:2048
	global_load_dwordx4 v[74:77], v[6:7], off offset:3072
	v_add_co_u32_e32 v2, vcc, 0x3000, v2
	s_lshl_b32 s2, s2, 12
	s_nop 0
	v_addc_co_u32_e32 v3, vcc, 0, v3, vcc
	global_load_dwordx4 v[78:81], v[2:3], off
	global_load_dwordx4 v[86:89], v[2:3], off offset:1024
	global_load_dwordx4 v[90:93], v[2:3], off offset:2048
	global_load_dwordx4 v[94:97], v[2:3], off offset:3072
	s_waitcnt lgkmcnt(0)
	s_barrier
	ds_read_b128 v[2:5], v113
	ds_read_b128 v[98:101], v113 offset:32
	ds_read_b128 v[22:25], v113 offset:16896
	ds_read_b128 v[102:105], v113 offset:16928
	s_and_b32 s2, s2, 0xf000
	s_add_u32 s0, s0, s2
	s_addc_u32 s1, s1, 0
	s_add_u32 s2, s6, s26
	s_addc_u32 s3, s7, 0
	v_cmp_eq_u32_e32 vcc, 0, v109
	s_waitcnt vmcnt(15) lgkmcnt(3)
	v_mfma_f32_32x32x16_f16 v[2:17], v[18:21], v[2:5], 0
	s_waitcnt lgkmcnt(1)
	v_mfma_f32_32x32x16_f16 v[18:33], v[18:21], v[22:25], 0
	s_waitcnt vmcnt(14)
	v_mfma_f32_32x32x16_f16 v[2:17], v[34:37], v[98:101], v[2:17]
	s_waitcnt lgkmcnt(0)
	v_mfma_f32_32x32x16_f16 v[18:33], v[34:37], v[102:105], v[18:33]
	ds_read_b128 v[34:37], v113 offset:64
	ds_read_b128 v[98:101], v113 offset:96
	s_waitcnt vmcnt(13) lgkmcnt(1)
	v_mfma_f32_32x32x16_f16 v[2:17], v[38:41], v[34:37], v[2:17]
	ds_read_b128 v[34:37], v113 offset:16960
	ds_read_b128 v[102:105], v113 offset:16992
	s_waitcnt lgkmcnt(1)
	v_mfma_f32_32x32x16_f16 v[18:33], v[38:41], v[34:37], v[18:33]
	ds_read_b128 v[34:37], v113 offset:128
	ds_read_b128 v[38:41], v113 offset:160
	s_waitcnt vmcnt(12)
	v_mfma_f32_32x32x16_f16 v[2:17], v[42:45], v[98:101], v[2:17]
	s_waitcnt lgkmcnt(2)
	v_mfma_f32_32x32x16_f16 v[18:33], v[42:45], v[102:105], v[18:33]
	s_waitcnt vmcnt(11) lgkmcnt(1)
	v_mfma_f32_32x32x16_f16 v[2:17], v[46:49], v[34:37], v[2:17]
	ds_read_b128 v[34:37], v113 offset:17024
	ds_read_b128 v[42:45], v113 offset:17056
	s_waitcnt lgkmcnt(1)
	v_mfma_f32_32x32x16_f16 v[18:33], v[46:49], v[34:37], v[18:33]
	s_waitcnt vmcnt(10)
	v_mfma_f32_32x32x16_f16 v[2:17], v[50:53], v[38:41], v[2:17]
	ds_read_b128 v[34:37], v113 offset:192
	ds_read_b128 v[38:41], v113 offset:224
	s_waitcnt lgkmcnt(2)
	v_mfma_f32_32x32x16_f16 v[18:33], v[50:53], v[42:45], v[18:33]
	s_waitcnt vmcnt(9) lgkmcnt(1)
	v_mfma_f32_32x32x16_f16 v[2:17], v[54:57], v[34:37], v[2:17]
	ds_read_b128 v[34:37], v113 offset:17088
	ds_read_b128 v[42:45], v113 offset:17120
	s_waitcnt lgkmcnt(1)
	v_mfma_f32_32x32x16_f16 v[18:33], v[54:57], v[34:37], v[18:33]
	s_waitcnt vmcnt(8)
	v_mfma_f32_32x32x16_f16 v[2:17], v[58:61], v[38:41], v[2:17]
	ds_read_b128 v[34:37], v113 offset:256
	ds_read_b128 v[38:41], v113 offset:288
	s_waitcnt lgkmcnt(2)
	v_mfma_f32_32x32x16_f16 v[18:33], v[58:61], v[42:45], v[18:33]
	s_waitcnt vmcnt(7) lgkmcnt(1)
	v_mfma_f32_32x32x16_f16 v[2:17], v[62:65], v[34:37], v[2:17]
	ds_read_b128 v[34:37], v113 offset:17152
	ds_read_b128 v[42:45], v113 offset:17184
	s_waitcnt lgkmcnt(1)
	v_mfma_f32_32x32x16_f16 v[18:33], v[62:65], v[34:37], v[18:33]
	s_waitcnt vmcnt(6)
	v_mfma_f32_32x32x16_f16 v[2:17], v[66:69], v[38:41], v[2:17]
	ds_read_b128 v[34:37], v113 offset:320
	ds_read_b128 v[38:41], v113 offset:352
	s_waitcnt lgkmcnt(2)
	v_mfma_f32_32x32x16_f16 v[18:33], v[66:69], v[42:45], v[18:33]
	s_waitcnt vmcnt(5) lgkmcnt(1)
	v_mfma_f32_32x32x16_f16 v[2:17], v[70:73], v[34:37], v[2:17]
	ds_read_b128 v[34:37], v113 offset:17216
	ds_read_b128 v[42:45], v113 offset:17248
	s_waitcnt lgkmcnt(1)
	v_mfma_f32_32x32x16_f16 v[18:33], v[70:73], v[34:37], v[18:33]
	s_waitcnt vmcnt(4)
	v_mfma_f32_32x32x16_f16 v[2:17], v[74:77], v[38:41], v[2:17]
	ds_read_b128 v[34:37], v113 offset:384
	ds_read_b128 v[38:41], v113 offset:416
	s_waitcnt lgkmcnt(2)
	v_mfma_f32_32x32x16_f16 v[18:33], v[74:77], v[42:45], v[18:33]
	s_waitcnt vmcnt(3) lgkmcnt(1)
	v_mfma_f32_32x32x16_f16 v[2:17], v[78:81], v[34:37], v[2:17]
	ds_read_b128 v[34:37], v113 offset:17280
	ds_read_b128 v[42:45], v113 offset:17312
	s_waitcnt lgkmcnt(1)
	v_mfma_f32_32x32x16_f16 v[18:33], v[78:81], v[34:37], v[18:33]
	s_waitcnt vmcnt(2)
	v_mfma_f32_32x32x16_f16 v[2:17], v[86:89], v[38:41], v[2:17]
	ds_read_b128 v[34:37], v113 offset:448
	ds_read_b128 v[38:41], v113 offset:480
	s_waitcnt lgkmcnt(2)
	v_mfma_f32_32x32x16_f16 v[18:33], v[86:89], v[42:45], v[18:33]
	s_waitcnt vmcnt(1) lgkmcnt(1)
	v_mfma_f32_32x32x16_f16 v[2:17], v[90:93], v[34:37], v[2:17]
	ds_read_b128 v[34:37], v113 offset:17344
	ds_read_b128 v[42:45], v113 offset:17376
	s_waitcnt lgkmcnt(0)
	s_barrier
	v_mfma_f32_32x32x16_f16 v[18:33], v[90:93], v[34:37], v[18:33]
	v_lshrrev_b32_e32 v34, 3, v0
	v_and_b32_e32 v34, 4, v34
	v_lshl_or_b32 v34, v107, 5, v34
	v_mul_u32_u24_e32 v34, 0x110, v34
	v_lshl_add_u32 v34, v112, 2, v34
	s_waitcnt vmcnt(0)
	v_mfma_f32_32x32x16_f16 v[2:17], v[94:97], v[38:41], v[2:17]
	v_mfma_f32_32x32x16_f16 v[18:33], v[94:97], v[42:45], v[18:33]
	s_nop 11
	ds_write2_b32 v34, v2, v18 offset1:32
	ds_write2_b32 v34, v3, v19 offset0:68 offset1:100
	ds_write2_b32 v34, v4, v20 offset0:136 offset1:168
	ds_write2_b32 v34, v5, v21 offset0:204 offset1:236
	v_add_u32_e32 v2, 0x800, v34
	ds_write2_b32 v2, v6, v22 offset0:32 offset1:64
	ds_write2_b32 v2, v7, v23 offset0:100 offset1:132
	ds_write2_b32 v2, v8, v24 offset0:168 offset1:200
	v_add_u32_e32 v2, 0xa00, v34
	ds_write2_b32 v2, v9, v25 offset0:108 offset1:140
	v_add_u32_e32 v2, 0x1000, v34
	ds_write2_b32 v2, v10, v26 offset0:64 offset1:96
	ds_write2_b32 v2, v11, v27 offset0:132 offset1:164
	ds_write2_b32 v2, v12, v28 offset0:200 offset1:232
	v_add_u32_e32 v2, 0x1400, v34
	ds_write2_b32 v2, v13, v29 offset0:12 offset1:44
	v_add_u32_e32 v2, 0x1800, v34
	v_and_b32_e32 v5, 60, v84
	v_mov_b32_e32 v8, 0x8800
	ds_write2_b32 v2, v14, v30 offset0:96 offset1:128
	ds_write2_b32 v2, v15, v31 offset0:164 offset1:196
	v_add_u32_e32 v2, 0x1a00, v34
	v_lshlrev_b32_e32 v6, 2, v5
	v_lshl_or_b32 v8, v82, 1, v8
	ds_write2_b32 v2, v16, v32 offset0:104 offset1:136
	v_add_u32_e32 v2, 0x1c00, v34
	v_add_u32_e32 v7, v6, v111
	v_mad_u32_u24 v9, v5, s4, v8
	ds_write2_b32 v2, v17, v33 offset0:44 offset1:76
	s_waitcnt lgkmcnt(0)
	s_barrier
	ds_read_b128 v[10:13], v7
	ds_read_u16 v14, v9
	ds_read_u16 v15, v9 offset:272
	ds_read_u16 v16, v9 offset:544
	ds_read_u16 v9, v9 offset:816
	v_or_b32_e32 v2, s20, v5
	v_mul_u32_u24_e32 v7, 0x110, v5
	s_waitcnt lgkmcnt(3)
	v_cvt_f32_f16_e32 v5, v14
	s_waitcnt lgkmcnt(2)
	v_cvt_f32_f16_e32 v14, v15
	s_waitcnt lgkmcnt(1)
	v_cvt_f32_f16_e32 v15, v16
	s_waitcnt lgkmcnt(0)
	v_cvt_f32_f16_e32 v9, v9
	v_or_b32_e32 v4, s8, v82
	v_ashrrev_i32_e32 v3, 31, v2
	v_add_f32_e32 v16, v10, v5
	v_ashrrev_i32_e32 v5, 31, v4
	v_lshl_add_u64 v[2:3], v[2:3], 1, s[2:3]
	v_add_f32_e32 v14, v11, v14
	v_add_f32_e32 v15, v12, v15
	v_add_f32_e32 v9, v13, v9
	v_lshlrev_b64 v[12:13], 13, v[4:5]
	v_cvt_pk_f16_f32 v11, v15, v9
	v_cvt_pk_f16_f32 v10, v16, v14
	v_lshl_add_u64 v[12:13], v[2:3], 0, v[12:13]
	global_store_dwordx2 v[12:13], v[10:11], off sc1
	v_mul_f32_e32 v11, v14, v14
	v_add_f32_e32 v10, v16, v14
	v_fmac_f32_e32 v11, v16, v16
	v_add_f32_e32 v10, v15, v10
	v_fmac_f32_e32 v11, v15, v15
	v_add_f32_e32 v10, v9, v10
	v_fmac_f32_e32 v11, v9, v9
	s_nop 0
	v_add_f32_dpp v9, v10, v10 quad_perm:[1,0,3,2] row_mask:0xf bank_mask:0xf bound_ctrl:1
	v_add_f32_dpp v11, v11, v11 quad_perm:[1,0,3,2] row_mask:0xf bank_mask:0xf bound_ctrl:1
	s_nop 0
	v_add_f32_dpp v9, v9, v9 quad_perm:[2,3,0,1] row_mask:0xf bank_mask:0xf bound_ctrl:1
	v_add_f32_dpp v11, v11, v11 quad_perm:[2,3,0,1] row_mask:0xf bank_mask:0xf bound_ctrl:1
	s_nop 0
	v_add_f32_dpp v9, v9, v9 row_half_mirror row_mask:0xf bank_mask:0xf bound_ctrl:1
	v_add_f32_dpp v11, v11, v11 row_half_mirror row_mask:0xf bank_mask:0xf bound_ctrl:1
	s_nop 0
	v_mov_b32_dpp v10, v9 row_mirror row_mask:0xf bank_mask:0xf bound_ctrl:1
	v_mov_b32_dpp v12, v11 row_mirror row_mask:0xf bank_mask:0xf bound_ctrl:1
	s_and_saveexec_b64 s[2:3], vcc
	s_cbranch_execz .LBB3_4
	v_lshl_add_u64 v[4:5], v[4:5], 2, s[0:1]
	v_add_f32_e32 v9, v9, v10
	v_add_f32_e32 v11, v11, v12
	global_atomic_add_f32 v[4:5], v9, off
	global_atomic_add_f32 v[4:5], v11, off offset:2048
